# adaLN prologue GEMV: 64 weight-row loads in flight per wave (two batches) instead of 8 per trip with a full drain; plus conv-in-router and dropped LDS waits
# speedup vs baseline: 1.0070x; 1.0003x over previous
; #define GAS __attribute__((address_space(1)))
; #define NTLD(P) (NT_STREAMS ? __builtin_nontemporal_load(P) : *(P))
; __device__ __forceinline__ void p0_prologue(Frame& F) {
;     ...
;         for (int item = (F.G == 256 ? (int)blockIdx.x : F.vcu); item < 192; item += F.G) {
;             const int layer = item / 96, col = (item % 96) * 64 + F.lane;
;             const float* W = inp(F, I_ADAW) + (size_t)layer * 1024 * 6144 + col;
;             float a[9];
; #pragma unroll
;             for (int r = 0; r < 9; ++r) a[r] = 0.f;
; #pragma unroll 8
;             for (int kk = 0; kk < 128; ++kk) { const int k = F.wave * 128 + kk; const float w = NTLD((const GAS float*)(W + (size_t)k * 6144));
; #pragma unroll
;                 for (int r = 0; r < 9; ++r) a[r] += sc[r * 1024 + k] * w; }
.LBB0_40:
	s_mul_hi_i32 s0, s9, 0x2aaaaaab
	ds_read_b64 v[4:5], v7
	s_lshr_b32 s1, s0, 31
	s_ashr_i32 s10, s0, 4
	s_add_i32 s10, s10, s1
	s_mul_i32 s0, s10, 0x60
	s_sub_i32 s0, s9, s0
	v_lshl_or_b32 v2, s0, 6, v35
	s_waitcnt lgkmcnt(0)
	v_readfirstlane_b32 s0, v4
	v_readfirstlane_b32 s1, v5
	s_add_u32 s0, s0, s13
	s_mul_i32 s5, s10, 0x1800000
	s_addc_u32 s1, s1, s16
	s_mul_hi_i32 s4, s10, 0x1800000
	s_add_u32 s0, s0, s5
	v_ashrrev_i32_e32 v3, 31, v2
	s_addc_u32 s1, s1, s4
	v_mov_b32_e32 v8, 0
	v_lshlrev_b32_e32 v4, 2, v2
	s_mov_b64 s[4:5], s[0:1]
	s_mov_b32 s11, s17
	v_mov_b32_e32 v9, v8
	v_mov_b32_e32 v10, v8
	v_mov_b32_e32 v11, v8
	v_mov_b32_e32 v12, v8
	v_mov_b32_e32 v13, v8
	v_mov_b32_e32 v14, v8
	v_mov_b32_e32 v15, v8
	v_mov_b32_e32 v16, v8
.Lada_pipe:
	global_load_dword v120, v4, s[4:5] nt
	s_add_u32 s4, s4, 0x6000
	s_addc_u32 s5, s5, 0
	global_load_dword v122, v4, s[4:5] nt
	s_add_u32 s4, s4, 0x6000
	s_addc_u32 s5, s5, 0
	global_load_dword v124, v4, s[4:5] nt
	s_add_u32 s4, s4, 0x6000
	s_addc_u32 s5, s5, 0
	global_load_dword v126, v4, s[4:5] nt
	s_add_u32 s4, s4, 0x6000
	s_addc_u32 s5, s5, 0
	global_load_dword v128, v4, s[4:5] nt
	s_add_u32 s4, s4, 0x6000
	s_addc_u32 s5, s5, 0
	global_load_dword v130, v4, s[4:5] nt
	s_add_u32 s4, s4, 0x6000
	s_addc_u32 s5, s5, 0
	global_load_dword v132, v4, s[4:5] nt
	s_add_u32 s4, s4, 0x6000
	s_addc_u32 s5, s5, 0
	global_load_dword v134, v4, s[4:5] nt
	s_add_u32 s4, s4, 0x6000
	s_addc_u32 s5, s5, 0
	global_load_dword v136, v4, s[4:5] nt
	s_add_u32 s4, s4, 0x6000
	s_addc_u32 s5, s5, 0
	global_load_dword v138, v4, s[4:5] nt
	s_add_u32 s4, s4, 0x6000
	s_addc_u32 s5, s5, 0
	global_load_dword v140, v4, s[4:5] nt
	s_add_u32 s4, s4, 0x6000
	s_addc_u32 s5, s5, 0
	global_load_dword v142, v4, s[4:5] nt
	s_add_u32 s4, s4, 0x6000
	s_addc_u32 s5, s5, 0
	global_load_dword v144, v4, s[4:5] nt
	s_add_u32 s4, s4, 0x6000
	s_addc_u32 s5, s5, 0
	global_load_dword v146, v4, s[4:5] nt
	s_add_u32 s4, s4, 0x6000
	s_addc_u32 s5, s5, 0
	global_load_dword v148, v4, s[4:5] nt
	s_add_u32 s4, s4, 0x6000
	s_addc_u32 s5, s5, 0
	global_load_dword v150, v4, s[4:5] nt
	s_add_u32 s4, s4, 0x6000
	s_addc_u32 s5, s5, 0
	global_load_dword v152, v4, s[4:5] nt
	s_add_u32 s4, s4, 0x6000
	s_addc_u32 s5, s5, 0
	global_load_dword v154, v4, s[4:5] nt
	s_add_u32 s4, s4, 0x6000
	s_addc_u32 s5, s5, 0
	global_load_dword v156, v4, s[4:5] nt
	s_add_u32 s4, s4, 0x6000
	s_addc_u32 s5, s5, 0
	global_load_dword v158, v4, s[4:5] nt
	s_add_u32 s4, s4, 0x6000
	s_addc_u32 s5, s5, 0
	global_load_dword v160, v4, s[4:5] nt
	s_add_u32 s4, s4, 0x6000
	s_addc_u32 s5, s5, 0
	global_load_dword v162, v4, s[4:5] nt
	s_add_u32 s4, s4, 0x6000
	s_addc_u32 s5, s5, 0
	global_load_dword v164, v4, s[4:5] nt
	s_add_u32 s4, s4, 0x6000
	s_addc_u32 s5, s5, 0
	global_load_dword v166, v4, s[4:5] nt
	s_add_u32 s4, s4, 0x6000
	s_addc_u32 s5, s5, 0
	global_load_dword v168, v4, s[4:5] nt
	s_add_u32 s4, s4, 0x6000
	s_addc_u32 s5, s5, 0
	global_load_dword v170, v4, s[4:5] nt
	s_add_u32 s4, s4, 0x6000
	s_addc_u32 s5, s5, 0
	global_load_dword v172, v4, s[4:5] nt
	s_add_u32 s4, s4, 0x6000
	s_addc_u32 s5, s5, 0
	global_load_dword v174, v4, s[4:5] nt
	s_add_u32 s4, s4, 0x6000
	s_addc_u32 s5, s5, 0
	global_load_dword v176, v4, s[4:5] nt
	s_add_u32 s4, s4, 0x6000
	s_addc_u32 s5, s5, 0
	global_load_dword v178, v4, s[4:5] nt
	s_add_u32 s4, s4, 0x6000
	s_addc_u32 s5, s5, 0
	global_load_dword v180, v4, s[4:5] nt
	s_add_u32 s4, s4, 0x6000
	s_addc_u32 s5, s5, 0
	global_load_dword v182, v4, s[4:5] nt
	s_add_u32 s4, s4, 0x6000
	s_addc_u32 s5, s5, 0
	global_load_dword v184, v4, s[4:5] nt
	s_add_u32 s4, s4, 0x6000
	s_addc_u32 s5, s5, 0
	global_load_dword v186, v4, s[4:5] nt
	s_add_u32 s4, s4, 0x6000
	s_addc_u32 s5, s5, 0
	global_load_dword v188, v4, s[4:5] nt
	s_add_u32 s4, s4, 0x6000
	s_addc_u32 s5, s5, 0
	global_load_dword v190, v4, s[4:5] nt
	s_add_u32 s4, s4, 0x6000
	s_addc_u32 s5, s5, 0
	global_load_dword v192, v4, s[4:5] nt
	s_add_u32 s4, s4, 0x6000
	s_addc_u32 s5, s5, 0
	global_load_dword v194, v4, s[4:5] nt
	s_add_u32 s4, s4, 0x6000
	s_addc_u32 s5, s5, 0
	global_load_dword v196, v4, s[4:5] nt
	s_add_u32 s4, s4, 0x6000
	s_addc_u32 s5, s5, 0
	global_load_dword v198, v4, s[4:5] nt
	s_add_u32 s4, s4, 0x6000
	s_addc_u32 s5, s5, 0
	global_load_dword v200, v4, s[4:5] nt
	s_add_u32 s4, s4, 0x6000
	s_addc_u32 s5, s5, 0
	global_load_dword v202, v4, s[4:5] nt
	s_add_u32 s4, s4, 0x6000
	s_addc_u32 s5, s5, 0
	global_load_dword v204, v4, s[4:5] nt
	s_add_u32 s4, s4, 0x6000
	s_addc_u32 s5, s5, 0
	global_load_dword v206, v4, s[4:5] nt
	s_add_u32 s4, s4, 0x6000
	s_addc_u32 s5, s5, 0
	global_load_dword v208, v4, s[4:5] nt
	s_add_u32 s4, s4, 0x6000
	s_addc_u32 s5, s5, 0
	global_load_dword v210, v4, s[4:5] nt
	s_add_u32 s4, s4, 0x6000
	s_addc_u32 s5, s5, 0
	global_load_dword v212, v4, s[4:5] nt
	s_add_u32 s4, s4, 0x6000
	s_addc_u32 s5, s5, 0
	global_load_dword v214, v4, s[4:5] nt
	s_add_u32 s4, s4, 0x6000
	s_addc_u32 s5, s5, 0
	global_load_dword v216, v4, s[4:5] nt
	s_add_u32 s4, s4, 0x6000
	s_addc_u32 s5, s5, 0
	global_load_dword v218, v4, s[4:5] nt
	s_add_u32 s4, s4, 0x6000
	s_addc_u32 s5, s5, 0
	global_load_dword v220, v4, s[4:5] nt
	s_add_u32 s4, s4, 0x6000
	s_addc_u32 s5, s5, 0
	global_load_dword v222, v4, s[4:5] nt
	s_add_u32 s4, s4, 0x6000
	s_addc_u32 s5, s5, 0
	global_load_dword v224, v4, s[4:5] nt
	s_add_u32 s4, s4, 0x6000
	s_addc_u32 s5, s5, 0
	global_load_dword v226, v4, s[4:5] nt
	s_add_u32 s4, s4, 0x6000
	s_addc_u32 s5, s5, 0
	global_load_dword v228, v4, s[4:5] nt
	s_add_u32 s4, s4, 0x6000
	s_addc_u32 s5, s5, 0
	global_load_dword v230, v4, s[4:5] nt
	s_add_u32 s4, s4, 0x6000
	s_addc_u32 s5, s5, 0
; #define GAS __attribute__((address_space(1)))
; #define NTLD(P) (NT_STREAMS ? __builtin_nontemporal_load(P) : *(P))
; __device__ __forceinline__ void p0_prologue(Frame& F) {
;     ...
; #pragma unroll 8
;             for (int kk = 0; kk < 128; ++kk) { const int k = F.wave * 128 + kk; const float w = NTLD((const GAS float*)(W + (size_t)k * 6144));
; #pragma unroll
;                 for (int r = 0; r < 9; ++r) a[r] += sc[r * 1024 + k] * w; }
	global_load_dword v232, v4, s[4:5] nt
	s_add_u32 s4, s4, 0x6000
	s_addc_u32 s5, s5, 0
	global_load_dword v234, v4, s[4:5] nt
	s_add_u32 s4, s4, 0x6000
	s_addc_u32 s5, s5, 0
	global_load_dword v236, v4, s[4:5] nt
	s_add_u32 s4, s4, 0x6000
	s_addc_u32 s5, s5, 0
	global_load_dword v238, v4, s[4:5] nt
	s_add_u32 s4, s4, 0x6000
	s_addc_u32 s5, s5, 0
	global_load_dword v240, v4, s[4:5] nt
	s_add_u32 s4, s4, 0x6000
	s_addc_u32 s5, s5, 0
	global_load_dword v242, v4, s[4:5] nt
	s_add_u32 s4, s4, 0x6000
	s_addc_u32 s5, s5, 0
	global_load_dword v244, v4, s[4:5] nt
	s_add_u32 s4, s4, 0x6000
	s_addc_u32 s5, s5, 0
	global_load_dword v246, v4, s[4:5] nt
	s_add_u32 s4, s4, 0x6000
	s_addc_u32 s5, s5, 0
	v_mov_b32_e32 v17, s11
	ds_read_b128 v[18:21], v17
	ds_read_b128 v[22:25], v17 offset:16
	ds_read_b128 v[26:29], v17 offset:4096
	ds_read_b128 v[30:33], v17 offset:4112
	ds_read_b128 v[36:39], v17 offset:8192
	ds_read_b128 v[40:43], v17 offset:8208
	ds_read_b128 v[44:47], v17 offset:12288
	ds_read_b128 v[48:51], v17 offset:12304
	ds_read_b128 v[52:55], v17 offset:16384
	ds_read_b128 v[56:59], v17 offset:16400
	ds_read_b128 v[60:63], v17 offset:20480
	ds_read_b128 v[64:67], v17 offset:20496
	ds_read_b128 v[68:71], v17 offset:24576
	ds_read_b128 v[72:75], v17 offset:24592
	ds_read_b128 v[76:79], v17 offset:28672
	ds_read_b128 v[80:83], v17 offset:28688
	s_add_i32 s11, s11, 32
	ds_read_b128 v[84:87], v17 offset:32768
	ds_read_b128 v[88:91], v17 offset:32784
	s_waitcnt lgkmcnt(0)
	v_mov_b32_e32 v92, v18
	v_mov_b32_e32 v93, v26
	v_mov_b32_e32 v26, v19
	v_mov_b32_e32 v18, v20
	v_mov_b32_e32 v19, v28
	v_mov_b32_e32 v28, v21
	s_waitcnt lgkmcnt(13)
	v_mov_b32_e32 v20, v36
	s_waitcnt lgkmcnt(11)
	v_mov_b32_e32 v21, v44
	v_mov_b32_e32 v44, v37
	v_mov_b32_e32 v36, v38
	v_mov_b32_e32 v37, v46
	v_mov_b32_e32 v46, v39
	s_waitcnt lgkmcnt(9)
	v_mov_b32_e32 v38, v52
	s_waitcnt lgkmcnt(7)
	v_mov_b32_e32 v39, v60
	v_mov_b32_e32 v60, v53
	v_mov_b32_e32 v52, v54
	v_mov_b32_e32 v53, v62
	v_mov_b32_e32 v62, v55
	s_waitcnt lgkmcnt(5)
	v_mov_b32_e32 v54, v68
	s_waitcnt lgkmcnt(3)
	v_mov_b32_e32 v55, v76
	v_mov_b32_e32 v76, v69
	v_mov_b32_e32 v68, v70
	v_mov_b32_e32 v69, v78
	v_mov_b32_e32 v78, v71
	v_mov_b32_e32 v70, v22
	v_mov_b32_e32 v71, v30
	v_mov_b32_e32 v30, v23
	v_mov_b32_e32 v22, v24
	v_mov_b32_e32 v23, v32
	v_mov_b32_e32 v32, v25
	v_mov_b32_e32 v24, v40
	v_mov_b32_e32 v25, v48
	v_mov_b32_e32 v48, v41
	v_mov_b32_e32 v40, v42
	v_mov_b32_e32 v41, v50
	v_mov_b32_e32 v50, v43
	v_mov_b32_e32 v42, v56
	v_mov_b32_e32 v43, v64
	v_mov_b32_e32 v64, v57
	v_mov_b32_e32 v56, v58
	v_mov_b32_e32 v57, v66
	v_mov_b32_e32 v66, v59
	v_mov_b32_e32 v58, v72
	s_waitcnt lgkmcnt(2)
	v_mov_b32_e32 v59, v80
	v_mov_b32_e32 v80, v73
	v_mov_b32_e32 v72, v74
	v_mov_b32_e32 v73, v82
	v_mov_b32_e32 v82, v75
	s_waitcnt vmcnt(63)
	v_pk_fma_f32 v[8:9], v[120:121], v[92:93], v[8:9] op_sel_hi:[0,1,1]
	v_pk_fma_f32 v[10:11], v[120:121], v[20:21], v[10:11] op_sel_hi:[0,1,1]
	v_pk_fma_f32 v[12:13], v[120:121], v[38:39], v[12:13] op_sel_hi:[0,1,1]
	v_pk_fma_f32 v[14:15], v[120:121], v[54:55], v[14:15] op_sel_hi:[0,1,1]
	s_waitcnt lgkmcnt(1)
	v_fmac_f32_e32 v16, v120, v84
	s_waitcnt vmcnt(62)
	v_pk_fma_f32 v[8:9], v[122:123], v[26:27], v[8:9] op_sel_hi:[0,1,1]
	v_pk_fma_f32 v[10:11], v[122:123], v[44:45], v[10:11] op_sel_hi:[0,1,1]
	v_pk_fma_f32 v[12:13], v[122:123], v[60:61], v[12:13] op_sel_hi:[0,1,1]
	v_pk_fma_f32 v[14:15], v[122:123], v[76:77], v[14:15] op_sel_hi:[0,1,1]
	v_fmac_f32_e32 v16, v122, v85
	s_waitcnt vmcnt(61)
	v_pk_fma_f32 v[8:9], v[124:125], v[18:19], v[8:9] op_sel_hi:[0,1,1]
	v_pk_fma_f32 v[10:11], v[124:125], v[36:37], v[10:11] op_sel_hi:[0,1,1]
	v_pk_fma_f32 v[12:13], v[124:125], v[52:53], v[12:13] op_sel_hi:[0,1,1]
	v_pk_fma_f32 v[14:15], v[124:125], v[68:69], v[14:15] op_sel_hi:[0,1,1]
	v_fmac_f32_e32 v16, v124, v86
	s_waitcnt vmcnt(60)
	v_pk_fma_f32 v[8:9], v[126:127], v[28:29], v[8:9] op_sel_hi:[0,1,1]
	v_pk_fma_f32 v[10:11], v[126:127], v[46:47], v[10:11] op_sel_hi:[0,1,1]
	v_pk_fma_f32 v[12:13], v[126:127], v[62:63], v[12:13] op_sel_hi:[0,1,1]
	v_pk_fma_f32 v[14:15], v[126:127], v[78:79], v[14:15] op_sel_hi:[0,1,1]
	v_fmac_f32_e32 v16, v126, v87
	s_waitcnt vmcnt(59)
	v_pk_fma_f32 v[8:9], v[128:129], v[70:71], v[8:9] op_sel_hi:[0,1,1]
	v_pk_fma_f32 v[10:11], v[128:129], v[24:25], v[10:11] op_sel_hi:[0,1,1]
	v_pk_fma_f32 v[12:13], v[128:129], v[42:43], v[12:13] op_sel_hi:[0,1,1]
	v_pk_fma_f32 v[14:15], v[128:129], v[58:59], v[14:15] op_sel_hi:[0,1,1]
	s_waitcnt lgkmcnt(0)
	v_fmac_f32_e32 v16, v128, v88
	s_waitcnt vmcnt(58)
	v_pk_fma_f32 v[8:9], v[130:131], v[30:31], v[8:9] op_sel_hi:[0,1,1]
	v_pk_fma_f32 v[10:11], v[130:131], v[48:49], v[10:11] op_sel_hi:[0,1,1]
	v_pk_fma_f32 v[12:13], v[130:131], v[64:65], v[12:13] op_sel_hi:[0,1,1]
	v_pk_fma_f32 v[14:15], v[130:131], v[80:81], v[14:15] op_sel_hi:[0,1,1]
	v_fmac_f32_e32 v16, v130, v89
	s_waitcnt vmcnt(57)
	v_pk_fma_f32 v[8:9], v[132:133], v[22:23], v[8:9] op_sel_hi:[0,1,1]
	v_pk_fma_f32 v[10:11], v[132:133], v[40:41], v[10:11] op_sel_hi:[0,1,1]
	v_pk_fma_f32 v[12:13], v[132:133], v[56:57], v[12:13] op_sel_hi:[0,1,1]
	v_pk_fma_f32 v[14:15], v[132:133], v[72:73], v[14:15] op_sel_hi:[0,1,1]
	v_fmac_f32_e32 v16, v132, v90
	s_waitcnt vmcnt(56)
; #define GAS __attribute__((address_space(1)))
; #define NTLD(P) (NT_STREAMS ? __builtin_nontemporal_load(P) : *(P))
; __device__ __forceinline__ void p0_prologue(Frame& F) {
;     ...
; #pragma unroll 8
;             for (int kk = 0; kk < 128; ++kk) { const int k = F.wave * 128 + kk; const float w = NTLD((const GAS float*)(W + (size_t)k * 6144));
; #pragma unroll
;                 for (int r = 0; r < 9; ++r) a[r] += sc[r * 1024 + k] * w; }
	v_pk_fma_f32 v[8:9], v[134:135], v[32:33], v[8:9] op_sel_hi:[0,1,1]
	v_pk_fma_f32 v[10:11], v[134:135], v[50:51], v[10:11] op_sel_hi:[0,1,1]
	v_pk_fma_f32 v[12:13], v[134:135], v[66:67], v[12:13] op_sel_hi:[0,1,1]
	v_pk_fma_f32 v[14:15], v[134:135], v[82:83], v[14:15] op_sel_hi:[0,1,1]
	v_fmac_f32_e32 v16, v134, v91
	v_mov_b32_e32 v17, s11
	ds_read_b128 v[18:21], v17
	ds_read_b128 v[22:25], v17 offset:16
	ds_read_b128 v[26:29], v17 offset:4096
	ds_read_b128 v[30:33], v17 offset:4112
	ds_read_b128 v[36:39], v17 offset:8192
	ds_read_b128 v[40:43], v17 offset:8208
	ds_read_b128 v[44:47], v17 offset:12288
	ds_read_b128 v[48:51], v17 offset:12304
	ds_read_b128 v[52:55], v17 offset:16384
	ds_read_b128 v[56:59], v17 offset:16400
	ds_read_b128 v[60:63], v17 offset:20480
	ds_read_b128 v[64:67], v17 offset:20496
	ds_read_b128 v[68:71], v17 offset:24576
	ds_read_b128 v[72:75], v17 offset:24592
	ds_read_b128 v[76:79], v17 offset:28672
	ds_read_b128 v[80:83], v17 offset:28688
	s_add_i32 s11, s11, 32
	ds_read_b128 v[84:87], v17 offset:32768
	ds_read_b128 v[88:91], v17 offset:32784
	s_waitcnt lgkmcnt(0)
	v_mov_b32_e32 v92, v18
	v_mov_b32_e32 v93, v26
	v_mov_b32_e32 v26, v19
	v_mov_b32_e32 v18, v20
	v_mov_b32_e32 v19, v28
	v_mov_b32_e32 v28, v21
	s_waitcnt lgkmcnt(13)
	v_mov_b32_e32 v20, v36
	s_waitcnt lgkmcnt(11)
	v_mov_b32_e32 v21, v44
	v_mov_b32_e32 v44, v37
	v_mov_b32_e32 v36, v38
	v_mov_b32_e32 v37, v46
	v_mov_b32_e32 v46, v39
	s_waitcnt lgkmcnt(9)
	v_mov_b32_e32 v38, v52
	s_waitcnt lgkmcnt(7)
	v_mov_b32_e32 v39, v60
	v_mov_b32_e32 v60, v53
	v_mov_b32_e32 v52, v54
	v_mov_b32_e32 v53, v62
	v_mov_b32_e32 v62, v55
	s_waitcnt lgkmcnt(5)
	v_mov_b32_e32 v54, v68
	s_waitcnt lgkmcnt(3)
	v_mov_b32_e32 v55, v76
	v_mov_b32_e32 v76, v69
	v_mov_b32_e32 v68, v70
	v_mov_b32_e32 v69, v78
	v_mov_b32_e32 v78, v71
	v_mov_b32_e32 v70, v22
	v_mov_b32_e32 v71, v30
	v_mov_b32_e32 v30, v23
	v_mov_b32_e32 v22, v24
	v_mov_b32_e32 v23, v32
	v_mov_b32_e32 v32, v25
	v_mov_b32_e32 v24, v40
	v_mov_b32_e32 v25, v48
	v_mov_b32_e32 v48, v41
	v_mov_b32_e32 v40, v42
	v_mov_b32_e32 v41, v50
	v_mov_b32_e32 v50, v43
	v_mov_b32_e32 v42, v56
	v_mov_b32_e32 v43, v64
	v_mov_b32_e32 v64, v57
	v_mov_b32_e32 v56, v58
	v_mov_b32_e32 v57, v66
	v_mov_b32_e32 v66, v59
	v_mov_b32_e32 v58, v72
	s_waitcnt lgkmcnt(2)
	v_mov_b32_e32 v59, v80
	v_mov_b32_e32 v80, v73
	v_mov_b32_e32 v72, v74
	v_mov_b32_e32 v73, v82
	v_mov_b32_e32 v82, v75
	s_waitcnt vmcnt(55)
	v_pk_fma_f32 v[8:9], v[136:137], v[92:93], v[8:9] op_sel_hi:[0,1,1]
	v_pk_fma_f32 v[10:11], v[136:137], v[20:21], v[10:11] op_sel_hi:[0,1,1]
	v_pk_fma_f32 v[12:13], v[136:137], v[38:39], v[12:13] op_sel_hi:[0,1,1]
	v_pk_fma_f32 v[14:15], v[136:137], v[54:55], v[14:15] op_sel_hi:[0,1,1]
	s_waitcnt lgkmcnt(1)
	v_fmac_f32_e32 v16, v136, v84
	s_waitcnt vmcnt(54)
	v_pk_fma_f32 v[8:9], v[138:139], v[26:27], v[8:9] op_sel_hi:[0,1,1]
	v_pk_fma_f32 v[10:11], v[138:139], v[44:45], v[10:11] op_sel_hi:[0,1,1]
	v_pk_fma_f32 v[12:13], v[138:139], v[60:61], v[12:13] op_sel_hi:[0,1,1]
	v_pk_fma_f32 v[14:15], v[138:139], v[76:77], v[14:15] op_sel_hi:[0,1,1]
	v_fmac_f32_e32 v16, v138, v85
	s_waitcnt vmcnt(53)
	v_pk_fma_f32 v[8:9], v[140:141], v[18:19], v[8:9] op_sel_hi:[0,1,1]
	v_pk_fma_f32 v[10:11], v[140:141], v[36:37], v[10:11] op_sel_hi:[0,1,1]
	v_pk_fma_f32 v[12:13], v[140:141], v[52:53], v[12:13] op_sel_hi:[0,1,1]
	v_pk_fma_f32 v[14:15], v[140:141], v[68:69], v[14:15] op_sel_hi:[0,1,1]
	v_fmac_f32_e32 v16, v140, v86
	s_waitcnt vmcnt(52)
	v_pk_fma_f32 v[8:9], v[142:143], v[28:29], v[8:9] op_sel_hi:[0,1,1]
	v_pk_fma_f32 v[10:11], v[142:143], v[46:47], v[10:11] op_sel_hi:[0,1,1]
	v_pk_fma_f32 v[12:13], v[142:143], v[62:63], v[12:13] op_sel_hi:[0,1,1]
	v_pk_fma_f32 v[14:15], v[142:143], v[78:79], v[14:15] op_sel_hi:[0,1,1]
	v_fmac_f32_e32 v16, v142, v87
	s_waitcnt vmcnt(51)
	v_pk_fma_f32 v[8:9], v[144:145], v[70:71], v[8:9] op_sel_hi:[0,1,1]
	v_pk_fma_f32 v[10:11], v[144:145], v[24:25], v[10:11] op_sel_hi:[0,1,1]
	v_pk_fma_f32 v[12:13], v[144:145], v[42:43], v[12:13] op_sel_hi:[0,1,1]
	v_pk_fma_f32 v[14:15], v[144:145], v[58:59], v[14:15] op_sel_hi:[0,1,1]
	s_waitcnt lgkmcnt(0)
	v_fmac_f32_e32 v16, v144, v88
	s_waitcnt vmcnt(50)
	v_pk_fma_f32 v[8:9], v[146:147], v[30:31], v[8:9] op_sel_hi:[0,1,1]
	v_pk_fma_f32 v[10:11], v[146:147], v[48:49], v[10:11] op_sel_hi:[0,1,1]
	v_pk_fma_f32 v[12:13], v[146:147], v[64:65], v[12:13] op_sel_hi:[0,1,1]
	v_pk_fma_f32 v[14:15], v[146:147], v[80:81], v[14:15] op_sel_hi:[0,1,1]
	v_fmac_f32_e32 v16, v146, v89
	s_waitcnt vmcnt(49)
	v_pk_fma_f32 v[8:9], v[148:149], v[22:23], v[8:9] op_sel_hi:[0,1,1]
	v_pk_fma_f32 v[10:11], v[148:149], v[40:41], v[10:11] op_sel_hi:[0,1,1]
	v_pk_fma_f32 v[12:13], v[148:149], v[56:57], v[12:13] op_sel_hi:[0,1,1]
	v_pk_fma_f32 v[14:15], v[148:149], v[72:73], v[14:15] op_sel_hi:[0,1,1]
	v_fmac_f32_e32 v16, v148, v90
	s_waitcnt vmcnt(48)
	v_pk_fma_f32 v[8:9], v[150:151], v[32:33], v[8:9] op_sel_hi:[0,1,1]
	v_pk_fma_f32 v[10:11], v[150:151], v[50:51], v[10:11] op_sel_hi:[0,1,1]
	v_pk_fma_f32 v[12:13], v[150:151], v[66:67], v[12:13] op_sel_hi:[0,1,1]
	v_pk_fma_f32 v[14:15], v[150:151], v[82:83], v[14:15] op_sel_hi:[0,1,1]
	v_fmac_f32_e32 v16, v150, v91
	v_mov_b32_e32 v17, s11
	ds_read_b128 v[18:21], v17
	ds_read_b128 v[22:25], v17 offset:16
	ds_read_b128 v[26:29], v17 offset:4096
	ds_read_b128 v[30:33], v17 offset:4112
	ds_read_b128 v[36:39], v17 offset:8192
	ds_read_b128 v[40:43], v17 offset:8208
	ds_read_b128 v[44:47], v17 offset:12288
	ds_read_b128 v[48:51], v17 offset:12304
	ds_read_b128 v[52:55], v17 offset:16384
	ds_read_b128 v[56:59], v17 offset:16400
	ds_read_b128 v[60:63], v17 offset:20480
	ds_read_b128 v[64:67], v17 offset:20496
	ds_read_b128 v[68:71], v17 offset:24576
	ds_read_b128 v[72:75], v17 offset:24592
	ds_read_b128 v[76:79], v17 offset:28672
	ds_read_b128 v[80:83], v17 offset:28688
	s_add_i32 s11, s11, 32
	ds_read_b128 v[84:87], v17 offset:32768
	ds_read_b128 v[88:91], v17 offset:32784
	s_waitcnt lgkmcnt(0)
; #define GAS __attribute__((address_space(1)))
; #define NTLD(P) (NT_STREAMS ? __builtin_nontemporal_load(P) : *(P))
; __device__ __forceinline__ void p0_prologue(Frame& F) {
;     ...
; #pragma unroll 8
;             for (int kk = 0; kk < 128; ++kk) { const int k = F.wave * 128 + kk; const float w = NTLD((const GAS float*)(W + (size_t)k * 6144));
; #pragma unroll
;                 for (int r = 0; r < 9; ++r) a[r] += sc[r * 1024 + k] * w; }
	v_mov_b32_e32 v92, v18
	v_mov_b32_e32 v93, v26
	v_mov_b32_e32 v26, v19
	v_mov_b32_e32 v18, v20
	v_mov_b32_e32 v19, v28
	v_mov_b32_e32 v28, v21
	s_waitcnt lgkmcnt(13)
	v_mov_b32_e32 v20, v36
	s_waitcnt lgkmcnt(11)
	v_mov_b32_e32 v21, v44
	v_mov_b32_e32 v44, v37
	v_mov_b32_e32 v36, v38
	v_mov_b32_e32 v37, v46
	v_mov_b32_e32 v46, v39
	s_waitcnt lgkmcnt(9)
	v_mov_b32_e32 v38, v52
	s_waitcnt lgkmcnt(7)
	v_mov_b32_e32 v39, v60
	v_mov_b32_e32 v60, v53
	v_mov_b32_e32 v52, v54
	v_mov_b32_e32 v53, v62
	v_mov_b32_e32 v62, v55
	s_waitcnt lgkmcnt(5)
	v_mov_b32_e32 v54, v68
	s_waitcnt lgkmcnt(3)
	v_mov_b32_e32 v55, v76
	v_mov_b32_e32 v76, v69
	v_mov_b32_e32 v68, v70
	v_mov_b32_e32 v69, v78
	v_mov_b32_e32 v78, v71
	v_mov_b32_e32 v70, v22
	v_mov_b32_e32 v71, v30
	v_mov_b32_e32 v30, v23
	v_mov_b32_e32 v22, v24
	v_mov_b32_e32 v23, v32
	v_mov_b32_e32 v32, v25
	v_mov_b32_e32 v24, v40
	v_mov_b32_e32 v25, v48
	v_mov_b32_e32 v48, v41
	v_mov_b32_e32 v40, v42
	v_mov_b32_e32 v41, v50
	v_mov_b32_e32 v50, v43
	v_mov_b32_e32 v42, v56
	v_mov_b32_e32 v43, v64
	v_mov_b32_e32 v64, v57
	v_mov_b32_e32 v56, v58
	v_mov_b32_e32 v57, v66
	v_mov_b32_e32 v66, v59
	v_mov_b32_e32 v58, v72
	s_waitcnt lgkmcnt(2)
	v_mov_b32_e32 v59, v80
	v_mov_b32_e32 v80, v73
	v_mov_b32_e32 v72, v74
	v_mov_b32_e32 v73, v82
	v_mov_b32_e32 v82, v75
	s_waitcnt vmcnt(47)
	v_pk_fma_f32 v[8:9], v[152:153], v[92:93], v[8:9] op_sel_hi:[0,1,1]
	v_pk_fma_f32 v[10:11], v[152:153], v[20:21], v[10:11] op_sel_hi:[0,1,1]
	v_pk_fma_f32 v[12:13], v[152:153], v[38:39], v[12:13] op_sel_hi:[0,1,1]
	v_pk_fma_f32 v[14:15], v[152:153], v[54:55], v[14:15] op_sel_hi:[0,1,1]
	s_waitcnt lgkmcnt(1)
	v_fmac_f32_e32 v16, v152, v84
	s_waitcnt vmcnt(46)
	v_pk_fma_f32 v[8:9], v[154:155], v[26:27], v[8:9] op_sel_hi:[0,1,1]
	v_pk_fma_f32 v[10:11], v[154:155], v[44:45], v[10:11] op_sel_hi:[0,1,1]
	v_pk_fma_f32 v[12:13], v[154:155], v[60:61], v[12:13] op_sel_hi:[0,1,1]
	v_pk_fma_f32 v[14:15], v[154:155], v[76:77], v[14:15] op_sel_hi:[0,1,1]
	v_fmac_f32_e32 v16, v154, v85
	s_waitcnt vmcnt(45)
	v_pk_fma_f32 v[8:9], v[156:157], v[18:19], v[8:9] op_sel_hi:[0,1,1]
	v_pk_fma_f32 v[10:11], v[156:157], v[36:37], v[10:11] op_sel_hi:[0,1,1]
	v_pk_fma_f32 v[12:13], v[156:157], v[52:53], v[12:13] op_sel_hi:[0,1,1]
	v_pk_fma_f32 v[14:15], v[156:157], v[68:69], v[14:15] op_sel_hi:[0,1,1]
	v_fmac_f32_e32 v16, v156, v86
	s_waitcnt vmcnt(44)
	v_pk_fma_f32 v[8:9], v[158:159], v[28:29], v[8:9] op_sel_hi:[0,1,1]
	v_pk_fma_f32 v[10:11], v[158:159], v[46:47], v[10:11] op_sel_hi:[0,1,1]
	v_pk_fma_f32 v[12:13], v[158:159], v[62:63], v[12:13] op_sel_hi:[0,1,1]
	v_pk_fma_f32 v[14:15], v[158:159], v[78:79], v[14:15] op_sel_hi:[0,1,1]
	v_fmac_f32_e32 v16, v158, v87
	s_waitcnt vmcnt(43)
	v_pk_fma_f32 v[8:9], v[160:161], v[70:71], v[8:9] op_sel_hi:[0,1,1]
	v_pk_fma_f32 v[10:11], v[160:161], v[24:25], v[10:11] op_sel_hi:[0,1,1]
	v_pk_fma_f32 v[12:13], v[160:161], v[42:43], v[12:13] op_sel_hi:[0,1,1]
	v_pk_fma_f32 v[14:15], v[160:161], v[58:59], v[14:15] op_sel_hi:[0,1,1]
	s_waitcnt lgkmcnt(0)
	v_fmac_f32_e32 v16, v160, v88
	s_waitcnt vmcnt(42)
	v_pk_fma_f32 v[8:9], v[162:163], v[30:31], v[8:9] op_sel_hi:[0,1,1]
	v_pk_fma_f32 v[10:11], v[162:163], v[48:49], v[10:11] op_sel_hi:[0,1,1]
	v_pk_fma_f32 v[12:13], v[162:163], v[64:65], v[12:13] op_sel_hi:[0,1,1]
	v_pk_fma_f32 v[14:15], v[162:163], v[80:81], v[14:15] op_sel_hi:[0,1,1]
	v_fmac_f32_e32 v16, v162, v89
	s_waitcnt vmcnt(41)
	v_pk_fma_f32 v[8:9], v[164:165], v[22:23], v[8:9] op_sel_hi:[0,1,1]
	v_pk_fma_f32 v[10:11], v[164:165], v[40:41], v[10:11] op_sel_hi:[0,1,1]
	v_pk_fma_f32 v[12:13], v[164:165], v[56:57], v[12:13] op_sel_hi:[0,1,1]
	v_pk_fma_f32 v[14:15], v[164:165], v[72:73], v[14:15] op_sel_hi:[0,1,1]
	v_fmac_f32_e32 v16, v164, v90
	s_waitcnt vmcnt(40)
	v_pk_fma_f32 v[8:9], v[166:167], v[32:33], v[8:9] op_sel_hi:[0,1,1]
	v_pk_fma_f32 v[10:11], v[166:167], v[50:51], v[10:11] op_sel_hi:[0,1,1]
	v_pk_fma_f32 v[12:13], v[166:167], v[66:67], v[12:13] op_sel_hi:[0,1,1]
	v_pk_fma_f32 v[14:15], v[166:167], v[82:83], v[14:15] op_sel_hi:[0,1,1]
	v_fmac_f32_e32 v16, v166, v91
	v_mov_b32_e32 v17, s11
	ds_read_b128 v[18:21], v17
	ds_read_b128 v[22:25], v17 offset:16
	ds_read_b128 v[26:29], v17 offset:4096
	ds_read_b128 v[30:33], v17 offset:4112
	ds_read_b128 v[36:39], v17 offset:8192
	ds_read_b128 v[40:43], v17 offset:8208
	ds_read_b128 v[44:47], v17 offset:12288
	ds_read_b128 v[48:51], v17 offset:12304
	ds_read_b128 v[52:55], v17 offset:16384
	ds_read_b128 v[56:59], v17 offset:16400
	ds_read_b128 v[60:63], v17 offset:20480
	ds_read_b128 v[64:67], v17 offset:20496
	ds_read_b128 v[68:71], v17 offset:24576
	ds_read_b128 v[72:75], v17 offset:24592
	ds_read_b128 v[76:79], v17 offset:28672
	ds_read_b128 v[80:83], v17 offset:28688
	s_add_i32 s11, s11, 32
	ds_read_b128 v[84:87], v17 offset:32768
	ds_read_b128 v[88:91], v17 offset:32784
	s_waitcnt lgkmcnt(0)
	v_mov_b32_e32 v92, v18
	v_mov_b32_e32 v93, v26
	v_mov_b32_e32 v26, v19
	v_mov_b32_e32 v18, v20
	v_mov_b32_e32 v19, v28
	v_mov_b32_e32 v28, v21
	s_waitcnt lgkmcnt(13)
	v_mov_b32_e32 v20, v36
	s_waitcnt lgkmcnt(11)
	v_mov_b32_e32 v21, v44
	v_mov_b32_e32 v44, v37
	v_mov_b32_e32 v36, v38
	v_mov_b32_e32 v37, v46
	v_mov_b32_e32 v46, v39
	s_waitcnt lgkmcnt(9)
	v_mov_b32_e32 v38, v52
	s_waitcnt lgkmcnt(7)
	v_mov_b32_e32 v39, v60
	v_mov_b32_e32 v60, v53
	v_mov_b32_e32 v52, v54
	v_mov_b32_e32 v53, v62
	v_mov_b32_e32 v62, v55
	s_waitcnt lgkmcnt(5)
	v_mov_b32_e32 v54, v68
	s_waitcnt lgkmcnt(3)
; #define GAS __attribute__((address_space(1)))
; #define NTLD(P) (NT_STREAMS ? __builtin_nontemporal_load(P) : *(P))
; __device__ __forceinline__ void p0_prologue(Frame& F) {
;     ...
; #pragma unroll 8
;             for (int kk = 0; kk < 128; ++kk) { const int k = F.wave * 128 + kk; const float w = NTLD((const GAS float*)(W + (size_t)k * 6144));
; #pragma unroll
;                 for (int r = 0; r < 9; ++r) a[r] += sc[r * 1024 + k] * w; }
	v_mov_b32_e32 v55, v76
	v_mov_b32_e32 v76, v69
	v_mov_b32_e32 v68, v70
	v_mov_b32_e32 v69, v78
	v_mov_b32_e32 v78, v71
	v_mov_b32_e32 v70, v22
	v_mov_b32_e32 v71, v30
	v_mov_b32_e32 v30, v23
	v_mov_b32_e32 v22, v24
	v_mov_b32_e32 v23, v32
	v_mov_b32_e32 v32, v25
	v_mov_b32_e32 v24, v40
	v_mov_b32_e32 v25, v48
	v_mov_b32_e32 v48, v41
	v_mov_b32_e32 v40, v42
	v_mov_b32_e32 v41, v50
	v_mov_b32_e32 v50, v43
	v_mov_b32_e32 v42, v56
	v_mov_b32_e32 v43, v64
	v_mov_b32_e32 v64, v57
	v_mov_b32_e32 v56, v58
	v_mov_b32_e32 v57, v66
	v_mov_b32_e32 v66, v59
	v_mov_b32_e32 v58, v72
	s_waitcnt lgkmcnt(2)
	v_mov_b32_e32 v59, v80
	v_mov_b32_e32 v80, v73
	v_mov_b32_e32 v72, v74
	v_mov_b32_e32 v73, v82
	v_mov_b32_e32 v82, v75
	s_waitcnt vmcnt(39)
	v_pk_fma_f32 v[8:9], v[168:169], v[92:93], v[8:9] op_sel_hi:[0,1,1]
	v_pk_fma_f32 v[10:11], v[168:169], v[20:21], v[10:11] op_sel_hi:[0,1,1]
	v_pk_fma_f32 v[12:13], v[168:169], v[38:39], v[12:13] op_sel_hi:[0,1,1]
	v_pk_fma_f32 v[14:15], v[168:169], v[54:55], v[14:15] op_sel_hi:[0,1,1]
	s_waitcnt lgkmcnt(1)
	v_fmac_f32_e32 v16, v168, v84
	s_waitcnt vmcnt(38)
	v_pk_fma_f32 v[8:9], v[170:171], v[26:27], v[8:9] op_sel_hi:[0,1,1]
	v_pk_fma_f32 v[10:11], v[170:171], v[44:45], v[10:11] op_sel_hi:[0,1,1]
	v_pk_fma_f32 v[12:13], v[170:171], v[60:61], v[12:13] op_sel_hi:[0,1,1]
	v_pk_fma_f32 v[14:15], v[170:171], v[76:77], v[14:15] op_sel_hi:[0,1,1]
	v_fmac_f32_e32 v16, v170, v85
	s_waitcnt vmcnt(37)
	v_pk_fma_f32 v[8:9], v[172:173], v[18:19], v[8:9] op_sel_hi:[0,1,1]
	v_pk_fma_f32 v[10:11], v[172:173], v[36:37], v[10:11] op_sel_hi:[0,1,1]
	v_pk_fma_f32 v[12:13], v[172:173], v[52:53], v[12:13] op_sel_hi:[0,1,1]
	v_pk_fma_f32 v[14:15], v[172:173], v[68:69], v[14:15] op_sel_hi:[0,1,1]
	v_fmac_f32_e32 v16, v172, v86
	s_waitcnt vmcnt(36)
	v_pk_fma_f32 v[8:9], v[174:175], v[28:29], v[8:9] op_sel_hi:[0,1,1]
	v_pk_fma_f32 v[10:11], v[174:175], v[46:47], v[10:11] op_sel_hi:[0,1,1]
	v_pk_fma_f32 v[12:13], v[174:175], v[62:63], v[12:13] op_sel_hi:[0,1,1]
	v_pk_fma_f32 v[14:15], v[174:175], v[78:79], v[14:15] op_sel_hi:[0,1,1]
	v_fmac_f32_e32 v16, v174, v87
	s_waitcnt vmcnt(35)
	v_pk_fma_f32 v[8:9], v[176:177], v[70:71], v[8:9] op_sel_hi:[0,1,1]
	v_pk_fma_f32 v[10:11], v[176:177], v[24:25], v[10:11] op_sel_hi:[0,1,1]
	v_pk_fma_f32 v[12:13], v[176:177], v[42:43], v[12:13] op_sel_hi:[0,1,1]
	v_pk_fma_f32 v[14:15], v[176:177], v[58:59], v[14:15] op_sel_hi:[0,1,1]
	s_waitcnt lgkmcnt(0)
	v_fmac_f32_e32 v16, v176, v88
	s_waitcnt vmcnt(34)
	v_pk_fma_f32 v[8:9], v[178:179], v[30:31], v[8:9] op_sel_hi:[0,1,1]
	v_pk_fma_f32 v[10:11], v[178:179], v[48:49], v[10:11] op_sel_hi:[0,1,1]
	v_pk_fma_f32 v[12:13], v[178:179], v[64:65], v[12:13] op_sel_hi:[0,1,1]
	v_pk_fma_f32 v[14:15], v[178:179], v[80:81], v[14:15] op_sel_hi:[0,1,1]
	v_fmac_f32_e32 v16, v178, v89
	s_waitcnt vmcnt(33)
	v_pk_fma_f32 v[8:9], v[180:181], v[22:23], v[8:9] op_sel_hi:[0,1,1]
	v_pk_fma_f32 v[10:11], v[180:181], v[40:41], v[10:11] op_sel_hi:[0,1,1]
	v_pk_fma_f32 v[12:13], v[180:181], v[56:57], v[12:13] op_sel_hi:[0,1,1]
	v_pk_fma_f32 v[14:15], v[180:181], v[72:73], v[14:15] op_sel_hi:[0,1,1]
	v_fmac_f32_e32 v16, v180, v90
	s_waitcnt vmcnt(32)
	v_pk_fma_f32 v[8:9], v[182:183], v[32:33], v[8:9] op_sel_hi:[0,1,1]
	v_pk_fma_f32 v[10:11], v[182:183], v[50:51], v[10:11] op_sel_hi:[0,1,1]
	v_pk_fma_f32 v[12:13], v[182:183], v[66:67], v[12:13] op_sel_hi:[0,1,1]
	v_pk_fma_f32 v[14:15], v[182:183], v[82:83], v[14:15] op_sel_hi:[0,1,1]
	v_fmac_f32_e32 v16, v182, v91
	v_mov_b32_e32 v17, s11
	ds_read_b128 v[18:21], v17
	ds_read_b128 v[22:25], v17 offset:16
	ds_read_b128 v[26:29], v17 offset:4096
	ds_read_b128 v[30:33], v17 offset:4112
	ds_read_b128 v[36:39], v17 offset:8192
	ds_read_b128 v[40:43], v17 offset:8208
	ds_read_b128 v[44:47], v17 offset:12288
	ds_read_b128 v[48:51], v17 offset:12304
	ds_read_b128 v[52:55], v17 offset:16384
	ds_read_b128 v[56:59], v17 offset:16400
	ds_read_b128 v[60:63], v17 offset:20480
	ds_read_b128 v[64:67], v17 offset:20496
	ds_read_b128 v[68:71], v17 offset:24576
	ds_read_b128 v[72:75], v17 offset:24592
	ds_read_b128 v[76:79], v17 offset:28672
	ds_read_b128 v[80:83], v17 offset:28688
	s_add_i32 s11, s11, 32
	ds_read_b128 v[84:87], v17 offset:32768
	ds_read_b128 v[88:91], v17 offset:32784
	s_waitcnt lgkmcnt(0)
	v_mov_b32_e32 v92, v18
	v_mov_b32_e32 v93, v26
	v_mov_b32_e32 v26, v19
	v_mov_b32_e32 v18, v20
	v_mov_b32_e32 v19, v28
	v_mov_b32_e32 v28, v21
	s_waitcnt lgkmcnt(13)
	v_mov_b32_e32 v20, v36
	s_waitcnt lgkmcnt(11)
	v_mov_b32_e32 v21, v44
	v_mov_b32_e32 v44, v37
	v_mov_b32_e32 v36, v38
	v_mov_b32_e32 v37, v46
	v_mov_b32_e32 v46, v39
	s_waitcnt lgkmcnt(9)
	v_mov_b32_e32 v38, v52
	s_waitcnt lgkmcnt(7)
	v_mov_b32_e32 v39, v60
	v_mov_b32_e32 v60, v53
	v_mov_b32_e32 v52, v54
	v_mov_b32_e32 v53, v62
	v_mov_b32_e32 v62, v55
	s_waitcnt lgkmcnt(5)
	v_mov_b32_e32 v54, v68
	s_waitcnt lgkmcnt(3)
	v_mov_b32_e32 v55, v76
	v_mov_b32_e32 v76, v69
	v_mov_b32_e32 v68, v70
	v_mov_b32_e32 v69, v78
	v_mov_b32_e32 v78, v71
	v_mov_b32_e32 v70, v22
	v_mov_b32_e32 v71, v30
	v_mov_b32_e32 v30, v23
	v_mov_b32_e32 v22, v24
	v_mov_b32_e32 v23, v32
	v_mov_b32_e32 v32, v25
	v_mov_b32_e32 v24, v40
	v_mov_b32_e32 v25, v48
	v_mov_b32_e32 v48, v41
	v_mov_b32_e32 v40, v42
	v_mov_b32_e32 v41, v50
	v_mov_b32_e32 v50, v43
	v_mov_b32_e32 v42, v56
	v_mov_b32_e32 v43, v64
	v_mov_b32_e32 v64, v57
	v_mov_b32_e32 v56, v58
	v_mov_b32_e32 v57, v66
	v_mov_b32_e32 v66, v59
	v_mov_b32_e32 v58, v72
	s_waitcnt lgkmcnt(2)
	v_mov_b32_e32 v59, v80
	v_mov_b32_e32 v80, v73
	v_mov_b32_e32 v72, v74
	v_mov_b32_e32 v73, v82
	v_mov_b32_e32 v82, v75
	s_waitcnt vmcnt(31)
; #define GAS __attribute__((address_space(1)))
; #define NTLD(P) (NT_STREAMS ? __builtin_nontemporal_load(P) : *(P))
; __device__ __forceinline__ void p0_prologue(Frame& F) {
;     ...
; #pragma unroll 8
;             for (int kk = 0; kk < 128; ++kk) { const int k = F.wave * 128 + kk; const float w = NTLD((const GAS float*)(W + (size_t)k * 6144));
; #pragma unroll
;                 for (int r = 0; r < 9; ++r) a[r] += sc[r * 1024 + k] * w; }
	v_pk_fma_f32 v[8:9], v[184:185], v[92:93], v[8:9] op_sel_hi:[0,1,1]
	v_pk_fma_f32 v[10:11], v[184:185], v[20:21], v[10:11] op_sel_hi:[0,1,1]
	v_pk_fma_f32 v[12:13], v[184:185], v[38:39], v[12:13] op_sel_hi:[0,1,1]
	v_pk_fma_f32 v[14:15], v[184:185], v[54:55], v[14:15] op_sel_hi:[0,1,1]
	s_waitcnt lgkmcnt(1)
	v_fmac_f32_e32 v16, v184, v84
	s_waitcnt vmcnt(30)
	v_pk_fma_f32 v[8:9], v[186:187], v[26:27], v[8:9] op_sel_hi:[0,1,1]
	v_pk_fma_f32 v[10:11], v[186:187], v[44:45], v[10:11] op_sel_hi:[0,1,1]
	v_pk_fma_f32 v[12:13], v[186:187], v[60:61], v[12:13] op_sel_hi:[0,1,1]
	v_pk_fma_f32 v[14:15], v[186:187], v[76:77], v[14:15] op_sel_hi:[0,1,1]
	v_fmac_f32_e32 v16, v186, v85
	s_waitcnt vmcnt(29)
	v_pk_fma_f32 v[8:9], v[188:189], v[18:19], v[8:9] op_sel_hi:[0,1,1]
	v_pk_fma_f32 v[10:11], v[188:189], v[36:37], v[10:11] op_sel_hi:[0,1,1]
	v_pk_fma_f32 v[12:13], v[188:189], v[52:53], v[12:13] op_sel_hi:[0,1,1]
	v_pk_fma_f32 v[14:15], v[188:189], v[68:69], v[14:15] op_sel_hi:[0,1,1]
	v_fmac_f32_e32 v16, v188, v86
	s_waitcnt vmcnt(28)
	v_pk_fma_f32 v[8:9], v[190:191], v[28:29], v[8:9] op_sel_hi:[0,1,1]
	v_pk_fma_f32 v[10:11], v[190:191], v[46:47], v[10:11] op_sel_hi:[0,1,1]
	v_pk_fma_f32 v[12:13], v[190:191], v[62:63], v[12:13] op_sel_hi:[0,1,1]
	v_pk_fma_f32 v[14:15], v[190:191], v[78:79], v[14:15] op_sel_hi:[0,1,1]
	v_fmac_f32_e32 v16, v190, v87
	s_waitcnt vmcnt(27)
	v_pk_fma_f32 v[8:9], v[192:193], v[70:71], v[8:9] op_sel_hi:[0,1,1]
	v_pk_fma_f32 v[10:11], v[192:193], v[24:25], v[10:11] op_sel_hi:[0,1,1]
	v_pk_fma_f32 v[12:13], v[192:193], v[42:43], v[12:13] op_sel_hi:[0,1,1]
	v_pk_fma_f32 v[14:15], v[192:193], v[58:59], v[14:15] op_sel_hi:[0,1,1]
	s_waitcnt lgkmcnt(0)
	v_fmac_f32_e32 v16, v192, v88
	s_waitcnt vmcnt(26)
	v_pk_fma_f32 v[8:9], v[194:195], v[30:31], v[8:9] op_sel_hi:[0,1,1]
	v_pk_fma_f32 v[10:11], v[194:195], v[48:49], v[10:11] op_sel_hi:[0,1,1]
	v_pk_fma_f32 v[12:13], v[194:195], v[64:65], v[12:13] op_sel_hi:[0,1,1]
	v_pk_fma_f32 v[14:15], v[194:195], v[80:81], v[14:15] op_sel_hi:[0,1,1]
	v_fmac_f32_e32 v16, v194, v89
	s_waitcnt vmcnt(25)
	v_pk_fma_f32 v[8:9], v[196:197], v[22:23], v[8:9] op_sel_hi:[0,1,1]
	v_pk_fma_f32 v[10:11], v[196:197], v[40:41], v[10:11] op_sel_hi:[0,1,1]
	v_pk_fma_f32 v[12:13], v[196:197], v[56:57], v[12:13] op_sel_hi:[0,1,1]
	v_pk_fma_f32 v[14:15], v[196:197], v[72:73], v[14:15] op_sel_hi:[0,1,1]
	v_fmac_f32_e32 v16, v196, v90
	s_waitcnt vmcnt(24)
	v_pk_fma_f32 v[8:9], v[198:199], v[32:33], v[8:9] op_sel_hi:[0,1,1]
	v_pk_fma_f32 v[10:11], v[198:199], v[50:51], v[10:11] op_sel_hi:[0,1,1]
	v_pk_fma_f32 v[12:13], v[198:199], v[66:67], v[12:13] op_sel_hi:[0,1,1]
	v_pk_fma_f32 v[14:15], v[198:199], v[82:83], v[14:15] op_sel_hi:[0,1,1]
	v_fmac_f32_e32 v16, v198, v91
	v_mov_b32_e32 v17, s11
	ds_read_b128 v[18:21], v17
	ds_read_b128 v[22:25], v17 offset:16
	ds_read_b128 v[26:29], v17 offset:4096
	ds_read_b128 v[30:33], v17 offset:4112
	ds_read_b128 v[36:39], v17 offset:8192
	ds_read_b128 v[40:43], v17 offset:8208
	ds_read_b128 v[44:47], v17 offset:12288
	ds_read_b128 v[48:51], v17 offset:12304
	ds_read_b128 v[52:55], v17 offset:16384
	ds_read_b128 v[56:59], v17 offset:16400
	ds_read_b128 v[60:63], v17 offset:20480
	ds_read_b128 v[64:67], v17 offset:20496
	ds_read_b128 v[68:71], v17 offset:24576
	ds_read_b128 v[72:75], v17 offset:24592
	ds_read_b128 v[76:79], v17 offset:28672
	ds_read_b128 v[80:83], v17 offset:28688
	s_add_i32 s11, s11, 32
	ds_read_b128 v[84:87], v17 offset:32768
	ds_read_b128 v[88:91], v17 offset:32784
	s_waitcnt lgkmcnt(0)
	v_mov_b32_e32 v92, v18
	v_mov_b32_e32 v93, v26
	v_mov_b32_e32 v26, v19
	v_mov_b32_e32 v18, v20
	v_mov_b32_e32 v19, v28
	v_mov_b32_e32 v28, v21
	s_waitcnt lgkmcnt(13)
	v_mov_b32_e32 v20, v36
	s_waitcnt lgkmcnt(11)
	v_mov_b32_e32 v21, v44
	v_mov_b32_e32 v44, v37
	v_mov_b32_e32 v36, v38
	v_mov_b32_e32 v37, v46
	v_mov_b32_e32 v46, v39
	s_waitcnt lgkmcnt(9)
	v_mov_b32_e32 v38, v52
	s_waitcnt lgkmcnt(7)
	v_mov_b32_e32 v39, v60
	v_mov_b32_e32 v60, v53
	v_mov_b32_e32 v52, v54
	v_mov_b32_e32 v53, v62
	v_mov_b32_e32 v62, v55
	s_waitcnt lgkmcnt(5)
	v_mov_b32_e32 v54, v68
	s_waitcnt lgkmcnt(3)
	v_mov_b32_e32 v55, v76
	v_mov_b32_e32 v76, v69
	v_mov_b32_e32 v68, v70
	v_mov_b32_e32 v69, v78
	v_mov_b32_e32 v78, v71
	v_mov_b32_e32 v70, v22
	v_mov_b32_e32 v71, v30
	v_mov_b32_e32 v30, v23
	v_mov_b32_e32 v22, v24
	v_mov_b32_e32 v23, v32
	v_mov_b32_e32 v32, v25
	v_mov_b32_e32 v24, v40
	v_mov_b32_e32 v25, v48
	v_mov_b32_e32 v48, v41
	v_mov_b32_e32 v40, v42
	v_mov_b32_e32 v41, v50
	v_mov_b32_e32 v50, v43
	v_mov_b32_e32 v42, v56
	v_mov_b32_e32 v43, v64
	v_mov_b32_e32 v64, v57
	v_mov_b32_e32 v56, v58
	v_mov_b32_e32 v57, v66
	v_mov_b32_e32 v66, v59
	v_mov_b32_e32 v58, v72
	s_waitcnt lgkmcnt(2)
	v_mov_b32_e32 v59, v80
	v_mov_b32_e32 v80, v73
	v_mov_b32_e32 v72, v74
	v_mov_b32_e32 v73, v82
	v_mov_b32_e32 v82, v75
	s_waitcnt vmcnt(23)
	v_pk_fma_f32 v[8:9], v[200:201], v[92:93], v[8:9] op_sel_hi:[0,1,1]
	v_pk_fma_f32 v[10:11], v[200:201], v[20:21], v[10:11] op_sel_hi:[0,1,1]
	v_pk_fma_f32 v[12:13], v[200:201], v[38:39], v[12:13] op_sel_hi:[0,1,1]
	v_pk_fma_f32 v[14:15], v[200:201], v[54:55], v[14:15] op_sel_hi:[0,1,1]
	s_waitcnt lgkmcnt(1)
	v_fmac_f32_e32 v16, v200, v84
	s_waitcnt vmcnt(22)
	v_pk_fma_f32 v[8:9], v[202:203], v[26:27], v[8:9] op_sel_hi:[0,1,1]
	v_pk_fma_f32 v[10:11], v[202:203], v[44:45], v[10:11] op_sel_hi:[0,1,1]
	v_pk_fma_f32 v[12:13], v[202:203], v[60:61], v[12:13] op_sel_hi:[0,1,1]
	v_pk_fma_f32 v[14:15], v[202:203], v[76:77], v[14:15] op_sel_hi:[0,1,1]
	v_fmac_f32_e32 v16, v202, v85
	s_waitcnt vmcnt(21)
; #define GAS __attribute__((address_space(1)))
; #define NTLD(P) (NT_STREAMS ? __builtin_nontemporal_load(P) : *(P))
; __device__ __forceinline__ void p0_prologue(Frame& F) {
;     ...
; #pragma unroll 8
;             for (int kk = 0; kk < 128; ++kk) { const int k = F.wave * 128 + kk; const float w = NTLD((const GAS float*)(W + (size_t)k * 6144));
; #pragma unroll
;                 for (int r = 0; r < 9; ++r) a[r] += sc[r * 1024 + k] * w; }
	v_pk_fma_f32 v[8:9], v[204:205], v[18:19], v[8:9] op_sel_hi:[0,1,1]
	v_pk_fma_f32 v[10:11], v[204:205], v[36:37], v[10:11] op_sel_hi:[0,1,1]
	v_pk_fma_f32 v[12:13], v[204:205], v[52:53], v[12:13] op_sel_hi:[0,1,1]
	v_pk_fma_f32 v[14:15], v[204:205], v[68:69], v[14:15] op_sel_hi:[0,1,1]
	v_fmac_f32_e32 v16, v204, v86
	s_waitcnt vmcnt(20)
	v_pk_fma_f32 v[8:9], v[206:207], v[28:29], v[8:9] op_sel_hi:[0,1,1]
	v_pk_fma_f32 v[10:11], v[206:207], v[46:47], v[10:11] op_sel_hi:[0,1,1]
	v_pk_fma_f32 v[12:13], v[206:207], v[62:63], v[12:13] op_sel_hi:[0,1,1]
	v_pk_fma_f32 v[14:15], v[206:207], v[78:79], v[14:15] op_sel_hi:[0,1,1]
	v_fmac_f32_e32 v16, v206, v87
	s_waitcnt vmcnt(19)
	v_pk_fma_f32 v[8:9], v[208:209], v[70:71], v[8:9] op_sel_hi:[0,1,1]
	v_pk_fma_f32 v[10:11], v[208:209], v[24:25], v[10:11] op_sel_hi:[0,1,1]
	v_pk_fma_f32 v[12:13], v[208:209], v[42:43], v[12:13] op_sel_hi:[0,1,1]
	v_pk_fma_f32 v[14:15], v[208:209], v[58:59], v[14:15] op_sel_hi:[0,1,1]
	s_waitcnt lgkmcnt(0)
	v_fmac_f32_e32 v16, v208, v88
	s_waitcnt vmcnt(18)
	v_pk_fma_f32 v[8:9], v[210:211], v[30:31], v[8:9] op_sel_hi:[0,1,1]
	v_pk_fma_f32 v[10:11], v[210:211], v[48:49], v[10:11] op_sel_hi:[0,1,1]
	v_pk_fma_f32 v[12:13], v[210:211], v[64:65], v[12:13] op_sel_hi:[0,1,1]
	v_pk_fma_f32 v[14:15], v[210:211], v[80:81], v[14:15] op_sel_hi:[0,1,1]
	v_fmac_f32_e32 v16, v210, v89
	s_waitcnt vmcnt(17)
	v_pk_fma_f32 v[8:9], v[212:213], v[22:23], v[8:9] op_sel_hi:[0,1,1]
	v_pk_fma_f32 v[10:11], v[212:213], v[40:41], v[10:11] op_sel_hi:[0,1,1]
	v_pk_fma_f32 v[12:13], v[212:213], v[56:57], v[12:13] op_sel_hi:[0,1,1]
	v_pk_fma_f32 v[14:15], v[212:213], v[72:73], v[14:15] op_sel_hi:[0,1,1]
	v_fmac_f32_e32 v16, v212, v90
	s_waitcnt vmcnt(16)
	v_pk_fma_f32 v[8:9], v[214:215], v[32:33], v[8:9] op_sel_hi:[0,1,1]
	v_pk_fma_f32 v[10:11], v[214:215], v[50:51], v[10:11] op_sel_hi:[0,1,1]
	v_pk_fma_f32 v[12:13], v[214:215], v[66:67], v[12:13] op_sel_hi:[0,1,1]
	v_pk_fma_f32 v[14:15], v[214:215], v[82:83], v[14:15] op_sel_hi:[0,1,1]
	v_fmac_f32_e32 v16, v214, v91
	v_mov_b32_e32 v17, s11
	ds_read_b128 v[18:21], v17
	ds_read_b128 v[22:25], v17 offset:16
	ds_read_b128 v[26:29], v17 offset:4096
	ds_read_b128 v[30:33], v17 offset:4112
	ds_read_b128 v[36:39], v17 offset:8192
	ds_read_b128 v[40:43], v17 offset:8208
	ds_read_b128 v[44:47], v17 offset:12288
	ds_read_b128 v[48:51], v17 offset:12304
	ds_read_b128 v[52:55], v17 offset:16384
	ds_read_b128 v[56:59], v17 offset:16400
	ds_read_b128 v[60:63], v17 offset:20480
	ds_read_b128 v[64:67], v17 offset:20496
	ds_read_b128 v[68:71], v17 offset:24576
	ds_read_b128 v[72:75], v17 offset:24592
	ds_read_b128 v[76:79], v17 offset:28672
	ds_read_b128 v[80:83], v17 offset:28688
	s_add_i32 s11, s11, 32
	ds_read_b128 v[84:87], v17 offset:32768
	ds_read_b128 v[88:91], v17 offset:32784
	s_waitcnt lgkmcnt(0)
	v_mov_b32_e32 v92, v18
	v_mov_b32_e32 v93, v26
	v_mov_b32_e32 v26, v19
	v_mov_b32_e32 v18, v20
	v_mov_b32_e32 v19, v28
	v_mov_b32_e32 v28, v21
	s_waitcnt lgkmcnt(13)
	v_mov_b32_e32 v20, v36
	s_waitcnt lgkmcnt(11)
	v_mov_b32_e32 v21, v44
	v_mov_b32_e32 v44, v37
	v_mov_b32_e32 v36, v38
	v_mov_b32_e32 v37, v46
	v_mov_b32_e32 v46, v39
	s_waitcnt lgkmcnt(9)
	v_mov_b32_e32 v38, v52
	s_waitcnt lgkmcnt(7)
	v_mov_b32_e32 v39, v60
	v_mov_b32_e32 v60, v53
	v_mov_b32_e32 v52, v54
	v_mov_b32_e32 v53, v62
	v_mov_b32_e32 v62, v55
	s_waitcnt lgkmcnt(5)
	v_mov_b32_e32 v54, v68
	s_waitcnt lgkmcnt(3)
	v_mov_b32_e32 v55, v76
	v_mov_b32_e32 v76, v69
	v_mov_b32_e32 v68, v70
	v_mov_b32_e32 v69, v78
	v_mov_b32_e32 v78, v71
	v_mov_b32_e32 v70, v22
	v_mov_b32_e32 v71, v30
	v_mov_b32_e32 v30, v23
	v_mov_b32_e32 v22, v24
	v_mov_b32_e32 v23, v32
	v_mov_b32_e32 v32, v25
	v_mov_b32_e32 v24, v40
	v_mov_b32_e32 v25, v48
	v_mov_b32_e32 v48, v41
	v_mov_b32_e32 v40, v42
	v_mov_b32_e32 v41, v50
	v_mov_b32_e32 v50, v43
	v_mov_b32_e32 v42, v56
	v_mov_b32_e32 v43, v64
	v_mov_b32_e32 v64, v57
	v_mov_b32_e32 v56, v58
	v_mov_b32_e32 v57, v66
	v_mov_b32_e32 v66, v59
	v_mov_b32_e32 v58, v72
	s_waitcnt lgkmcnt(2)
	v_mov_b32_e32 v59, v80
	v_mov_b32_e32 v80, v73
	v_mov_b32_e32 v72, v74
	v_mov_b32_e32 v73, v82
	v_mov_b32_e32 v82, v75
	s_waitcnt vmcnt(15)
	v_pk_fma_f32 v[8:9], v[216:217], v[92:93], v[8:9] op_sel_hi:[0,1,1]
	v_pk_fma_f32 v[10:11], v[216:217], v[20:21], v[10:11] op_sel_hi:[0,1,1]
	v_pk_fma_f32 v[12:13], v[216:217], v[38:39], v[12:13] op_sel_hi:[0,1,1]
	v_pk_fma_f32 v[14:15], v[216:217], v[54:55], v[14:15] op_sel_hi:[0,1,1]
	s_waitcnt lgkmcnt(1)
	v_fmac_f32_e32 v16, v216, v84
	s_waitcnt vmcnt(14)
	v_pk_fma_f32 v[8:9], v[218:219], v[26:27], v[8:9] op_sel_hi:[0,1,1]
	v_pk_fma_f32 v[10:11], v[218:219], v[44:45], v[10:11] op_sel_hi:[0,1,1]
	v_pk_fma_f32 v[12:13], v[218:219], v[60:61], v[12:13] op_sel_hi:[0,1,1]
	v_pk_fma_f32 v[14:15], v[218:219], v[76:77], v[14:15] op_sel_hi:[0,1,1]
	v_fmac_f32_e32 v16, v218, v85
	s_waitcnt vmcnt(13)
	v_pk_fma_f32 v[8:9], v[220:221], v[18:19], v[8:9] op_sel_hi:[0,1,1]
	v_pk_fma_f32 v[10:11], v[220:221], v[36:37], v[10:11] op_sel_hi:[0,1,1]
	v_pk_fma_f32 v[12:13], v[220:221], v[52:53], v[12:13] op_sel_hi:[0,1,1]
	v_pk_fma_f32 v[14:15], v[220:221], v[68:69], v[14:15] op_sel_hi:[0,1,1]
	v_fmac_f32_e32 v16, v220, v86
	s_waitcnt vmcnt(12)
	v_pk_fma_f32 v[8:9], v[222:223], v[28:29], v[8:9] op_sel_hi:[0,1,1]
	v_pk_fma_f32 v[10:11], v[222:223], v[46:47], v[10:11] op_sel_hi:[0,1,1]
	v_pk_fma_f32 v[12:13], v[222:223], v[62:63], v[12:13] op_sel_hi:[0,1,1]
	v_pk_fma_f32 v[14:15], v[222:223], v[78:79], v[14:15] op_sel_hi:[0,1,1]
	v_fmac_f32_e32 v16, v222, v87
	s_waitcnt vmcnt(11)
; #define GAS __attribute__((address_space(1)))
; #define NTLD(P) (NT_STREAMS ? __builtin_nontemporal_load(P) : *(P))
; __device__ __forceinline__ void p0_prologue(Frame& F) {
;     ...
; #pragma unroll 8
;             for (int kk = 0; kk < 128; ++kk) { const int k = F.wave * 128 + kk; const float w = NTLD((const GAS float*)(W + (size_t)k * 6144));
; #pragma unroll
;                 for (int r = 0; r < 9; ++r) a[r] += sc[r * 1024 + k] * w; }
	v_pk_fma_f32 v[8:9], v[224:225], v[70:71], v[8:9] op_sel_hi:[0,1,1]
	v_pk_fma_f32 v[10:11], v[224:225], v[24:25], v[10:11] op_sel_hi:[0,1,1]
	v_pk_fma_f32 v[12:13], v[224:225], v[42:43], v[12:13] op_sel_hi:[0,1,1]
	v_pk_fma_f32 v[14:15], v[224:225], v[58:59], v[14:15] op_sel_hi:[0,1,1]
	s_waitcnt lgkmcnt(0)
	v_fmac_f32_e32 v16, v224, v88
	s_waitcnt vmcnt(10)
	v_pk_fma_f32 v[8:9], v[226:227], v[30:31], v[8:9] op_sel_hi:[0,1,1]
	v_pk_fma_f32 v[10:11], v[226:227], v[48:49], v[10:11] op_sel_hi:[0,1,1]
	v_pk_fma_f32 v[12:13], v[226:227], v[64:65], v[12:13] op_sel_hi:[0,1,1]
	v_pk_fma_f32 v[14:15], v[226:227], v[80:81], v[14:15] op_sel_hi:[0,1,1]
	v_fmac_f32_e32 v16, v226, v89
	s_waitcnt vmcnt(9)
	v_pk_fma_f32 v[8:9], v[228:229], v[22:23], v[8:9] op_sel_hi:[0,1,1]
	v_pk_fma_f32 v[10:11], v[228:229], v[40:41], v[10:11] op_sel_hi:[0,1,1]
	v_pk_fma_f32 v[12:13], v[228:229], v[56:57], v[12:13] op_sel_hi:[0,1,1]
	v_pk_fma_f32 v[14:15], v[228:229], v[72:73], v[14:15] op_sel_hi:[0,1,1]
	v_fmac_f32_e32 v16, v228, v90
	s_waitcnt vmcnt(8)
	v_pk_fma_f32 v[8:9], v[230:231], v[32:33], v[8:9] op_sel_hi:[0,1,1]
	v_pk_fma_f32 v[10:11], v[230:231], v[50:51], v[10:11] op_sel_hi:[0,1,1]
	v_pk_fma_f32 v[12:13], v[230:231], v[66:67], v[12:13] op_sel_hi:[0,1,1]
	v_pk_fma_f32 v[14:15], v[230:231], v[82:83], v[14:15] op_sel_hi:[0,1,1]
	v_fmac_f32_e32 v16, v230, v91
	v_mov_b32_e32 v17, s11
	ds_read_b128 v[18:21], v17
	ds_read_b128 v[22:25], v17 offset:16
	ds_read_b128 v[26:29], v17 offset:4096
	ds_read_b128 v[30:33], v17 offset:4112
	ds_read_b128 v[36:39], v17 offset:8192
	ds_read_b128 v[40:43], v17 offset:8208
	ds_read_b128 v[44:47], v17 offset:12288
	ds_read_b128 v[48:51], v17 offset:12304
	ds_read_b128 v[52:55], v17 offset:16384
	ds_read_b128 v[56:59], v17 offset:16400
	ds_read_b128 v[60:63], v17 offset:20480
	ds_read_b128 v[64:67], v17 offset:20496
	ds_read_b128 v[68:71], v17 offset:24576
	ds_read_b128 v[72:75], v17 offset:24592
	ds_read_b128 v[76:79], v17 offset:28672
	ds_read_b128 v[80:83], v17 offset:28688
	s_add_i32 s11, s11, 32
	ds_read_b128 v[84:87], v17 offset:32768
	ds_read_b128 v[88:91], v17 offset:32784
	s_waitcnt lgkmcnt(0)
	v_mov_b32_e32 v92, v18
	v_mov_b32_e32 v93, v26
	v_mov_b32_e32 v26, v19
	v_mov_b32_e32 v18, v20
	v_mov_b32_e32 v19, v28
	v_mov_b32_e32 v28, v21
	s_waitcnt lgkmcnt(13)
	v_mov_b32_e32 v20, v36
	s_waitcnt lgkmcnt(11)
	v_mov_b32_e32 v21, v44
	v_mov_b32_e32 v44, v37
	v_mov_b32_e32 v36, v38
	v_mov_b32_e32 v37, v46
	v_mov_b32_e32 v46, v39
	s_waitcnt lgkmcnt(9)
	v_mov_b32_e32 v38, v52
	s_waitcnt lgkmcnt(7)
	v_mov_b32_e32 v39, v60
	v_mov_b32_e32 v60, v53
	v_mov_b32_e32 v52, v54
	v_mov_b32_e32 v53, v62
	v_mov_b32_e32 v62, v55
	s_waitcnt lgkmcnt(5)
	v_mov_b32_e32 v54, v68
	s_waitcnt lgkmcnt(3)
	v_mov_b32_e32 v55, v76
	v_mov_b32_e32 v76, v69
	v_mov_b32_e32 v68, v70
	v_mov_b32_e32 v69, v78
	v_mov_b32_e32 v78, v71
	v_mov_b32_e32 v70, v22
	v_mov_b32_e32 v71, v30
	v_mov_b32_e32 v30, v23
	v_mov_b32_e32 v22, v24
	v_mov_b32_e32 v23, v32
	v_mov_b32_e32 v32, v25
	v_mov_b32_e32 v24, v40
	v_mov_b32_e32 v25, v48
	v_mov_b32_e32 v48, v41
	v_mov_b32_e32 v40, v42
	v_mov_b32_e32 v41, v50
	v_mov_b32_e32 v50, v43
	v_mov_b32_e32 v42, v56
	v_mov_b32_e32 v43, v64
	v_mov_b32_e32 v64, v57
	v_mov_b32_e32 v56, v58
	v_mov_b32_e32 v57, v66
	v_mov_b32_e32 v66, v59
	v_mov_b32_e32 v58, v72
	s_waitcnt lgkmcnt(2)
	v_mov_b32_e32 v59, v80
	v_mov_b32_e32 v80, v73
	v_mov_b32_e32 v72, v74
	v_mov_b32_e32 v73, v82
	v_mov_b32_e32 v82, v75
	s_waitcnt vmcnt(7)
	v_pk_fma_f32 v[8:9], v[232:233], v[92:93], v[8:9] op_sel_hi:[0,1,1]
	v_pk_fma_f32 v[10:11], v[232:233], v[20:21], v[10:11] op_sel_hi:[0,1,1]
	v_pk_fma_f32 v[12:13], v[232:233], v[38:39], v[12:13] op_sel_hi:[0,1,1]
	v_pk_fma_f32 v[14:15], v[232:233], v[54:55], v[14:15] op_sel_hi:[0,1,1]
	s_waitcnt lgkmcnt(1)
	v_fmac_f32_e32 v16, v232, v84
	s_waitcnt vmcnt(6)
	v_pk_fma_f32 v[8:9], v[234:235], v[26:27], v[8:9] op_sel_hi:[0,1,1]
	v_pk_fma_f32 v[10:11], v[234:235], v[44:45], v[10:11] op_sel_hi:[0,1,1]
	v_pk_fma_f32 v[12:13], v[234:235], v[60:61], v[12:13] op_sel_hi:[0,1,1]
	v_pk_fma_f32 v[14:15], v[234:235], v[76:77], v[14:15] op_sel_hi:[0,1,1]
	v_fmac_f32_e32 v16, v234, v85
	s_waitcnt vmcnt(5)
	v_pk_fma_f32 v[8:9], v[236:237], v[18:19], v[8:9] op_sel_hi:[0,1,1]
	v_pk_fma_f32 v[10:11], v[236:237], v[36:37], v[10:11] op_sel_hi:[0,1,1]
	v_pk_fma_f32 v[12:13], v[236:237], v[52:53], v[12:13] op_sel_hi:[0,1,1]
	v_pk_fma_f32 v[14:15], v[236:237], v[68:69], v[14:15] op_sel_hi:[0,1,1]
	v_fmac_f32_e32 v16, v236, v86
	s_waitcnt vmcnt(4)
	v_pk_fma_f32 v[8:9], v[238:239], v[28:29], v[8:9] op_sel_hi:[0,1,1]
	v_pk_fma_f32 v[10:11], v[238:239], v[46:47], v[10:11] op_sel_hi:[0,1,1]
	v_pk_fma_f32 v[12:13], v[238:239], v[62:63], v[12:13] op_sel_hi:[0,1,1]
	v_pk_fma_f32 v[14:15], v[238:239], v[78:79], v[14:15] op_sel_hi:[0,1,1]
	v_fmac_f32_e32 v16, v238, v87
	s_waitcnt vmcnt(3)
	v_pk_fma_f32 v[8:9], v[240:241], v[70:71], v[8:9] op_sel_hi:[0,1,1]
	v_pk_fma_f32 v[10:11], v[240:241], v[24:25], v[10:11] op_sel_hi:[0,1,1]
	v_pk_fma_f32 v[12:13], v[240:241], v[42:43], v[12:13] op_sel_hi:[0,1,1]
	v_pk_fma_f32 v[14:15], v[240:241], v[58:59], v[14:15] op_sel_hi:[0,1,1]
	s_waitcnt lgkmcnt(0)
	v_fmac_f32_e32 v16, v240, v88
	s_waitcnt vmcnt(2)
	v_pk_fma_f32 v[8:9], v[242:243], v[30:31], v[8:9] op_sel_hi:[0,1,1]
	v_pk_fma_f32 v[10:11], v[242:243], v[48:49], v[10:11] op_sel_hi:[0,1,1]
	v_pk_fma_f32 v[12:13], v[242:243], v[64:65], v[12:13] op_sel_hi:[0,1,1]
	v_pk_fma_f32 v[14:15], v[242:243], v[80:81], v[14:15] op_sel_hi:[0,1,1]
	v_fmac_f32_e32 v16, v242, v89
	s_waitcnt vmcnt(1)
; #define GAS __attribute__((address_space(1)))
; #define NTLD(P) (NT_STREAMS ? __builtin_nontemporal_load(P) : *(P))
; __device__ __forceinline__ void p0_prologue(Frame& F) {
;     ...
;             for (int kk = 0; kk < 128; ++kk) { const int k = F.wave * 128 + kk; const float w = NTLD((const GAS float*)(W + (size_t)k * 6144));
; #pragma unroll
;                 for (int r = 0; r < 9; ++r) a[r] += sc[r * 1024 + k] * w; }
	v_pk_fma_f32 v[8:9], v[244:245], v[22:23], v[8:9] op_sel_hi:[0,1,1]
	v_pk_fma_f32 v[10:11], v[244:245], v[40:41], v[10:11] op_sel_hi:[0,1,1]
	v_pk_fma_f32 v[12:13], v[244:245], v[56:57], v[12:13] op_sel_hi:[0,1,1]
	v_pk_fma_f32 v[14:15], v[244:245], v[72:73], v[14:15] op_sel_hi:[0,1,1]
	v_fmac_f32_e32 v16, v244, v90
	s_waitcnt vmcnt(0)
	v_pk_fma_f32 v[8:9], v[246:247], v[32:33], v[8:9] op_sel_hi:[0,1,1]
	v_pk_fma_f32 v[10:11], v[246:247], v[50:51], v[10:11] op_sel_hi:[0,1,1]
	v_pk_fma_f32 v[12:13], v[246:247], v[66:67], v[12:13] op_sel_hi:[0,1,1]
	v_pk_fma_f32 v[14:15], v[246:247], v[82:83], v[14:15] op_sel_hi:[0,1,1]
	v_fmac_f32_e32 v16, v246, v91
	global_load_dword v120, v4, s[4:5] nt
	s_add_u32 s4, s4, 0x6000
	s_addc_u32 s5, s5, 0
	global_load_dword v122, v4, s[4:5] nt
	s_add_u32 s4, s4, 0x6000
	s_addc_u32 s5, s5, 0
	global_load_dword v124, v4, s[4:5] nt
	s_add_u32 s4, s4, 0x6000
	s_addc_u32 s5, s5, 0
	global_load_dword v126, v4, s[4:5] nt
	s_add_u32 s4, s4, 0x6000
	s_addc_u32 s5, s5, 0
	global_load_dword v128, v4, s[4:5] nt
	s_add_u32 s4, s4, 0x6000
	s_addc_u32 s5, s5, 0
	global_load_dword v130, v4, s[4:5] nt
	s_add_u32 s4, s4, 0x6000
	s_addc_u32 s5, s5, 0
	global_load_dword v132, v4, s[4:5] nt
	s_add_u32 s4, s4, 0x6000
	s_addc_u32 s5, s5, 0
	global_load_dword v134, v4, s[4:5] nt
	s_add_u32 s4, s4, 0x6000
	s_addc_u32 s5, s5, 0
	global_load_dword v136, v4, s[4:5] nt
	s_add_u32 s4, s4, 0x6000
	s_addc_u32 s5, s5, 0
	global_load_dword v138, v4, s[4:5] nt
	s_add_u32 s4, s4, 0x6000
	s_addc_u32 s5, s5, 0
	global_load_dword v140, v4, s[4:5] nt
	s_add_u32 s4, s4, 0x6000
	s_addc_u32 s5, s5, 0
	global_load_dword v142, v4, s[4:5] nt
	s_add_u32 s4, s4, 0x6000
	s_addc_u32 s5, s5, 0
	global_load_dword v144, v4, s[4:5] nt
	s_add_u32 s4, s4, 0x6000
	s_addc_u32 s5, s5, 0
	global_load_dword v146, v4, s[4:5] nt
	s_add_u32 s4, s4, 0x6000
	s_addc_u32 s5, s5, 0
	global_load_dword v148, v4, s[4:5] nt
	s_add_u32 s4, s4, 0x6000
	s_addc_u32 s5, s5, 0
	global_load_dword v150, v4, s[4:5] nt
	s_add_u32 s4, s4, 0x6000
	s_addc_u32 s5, s5, 0
	global_load_dword v152, v4, s[4:5] nt
	s_add_u32 s4, s4, 0x6000
	s_addc_u32 s5, s5, 0
	global_load_dword v154, v4, s[4:5] nt
	s_add_u32 s4, s4, 0x6000
	s_addc_u32 s5, s5, 0
	global_load_dword v156, v4, s[4:5] nt
	s_add_u32 s4, s4, 0x6000
	s_addc_u32 s5, s5, 0
	global_load_dword v158, v4, s[4:5] nt
	s_add_u32 s4, s4, 0x6000
	s_addc_u32 s5, s5, 0
	global_load_dword v160, v4, s[4:5] nt
	s_add_u32 s4, s4, 0x6000
	s_addc_u32 s5, s5, 0
	global_load_dword v162, v4, s[4:5] nt
	s_add_u32 s4, s4, 0x6000
	s_addc_u32 s5, s5, 0
	global_load_dword v164, v4, s[4:5] nt
	s_add_u32 s4, s4, 0x6000
	s_addc_u32 s5, s5, 0
	global_load_dword v166, v4, s[4:5] nt
	s_add_u32 s4, s4, 0x6000
	s_addc_u32 s5, s5, 0
	global_load_dword v168, v4, s[4:5] nt
	s_add_u32 s4, s4, 0x6000
	s_addc_u32 s5, s5, 0
	global_load_dword v170, v4, s[4:5] nt
	s_add_u32 s4, s4, 0x6000
	s_addc_u32 s5, s5, 0
	global_load_dword v172, v4, s[4:5] nt
	s_add_u32 s4, s4, 0x6000
	s_addc_u32 s5, s5, 0
	global_load_dword v174, v4, s[4:5] nt
	s_add_u32 s4, s4, 0x6000
	s_addc_u32 s5, s5, 0
	global_load_dword v176, v4, s[4:5] nt
	s_add_u32 s4, s4, 0x6000
	s_addc_u32 s5, s5, 0
	global_load_dword v178, v4, s[4:5] nt
	s_add_u32 s4, s4, 0x6000
	s_addc_u32 s5, s5, 0
	global_load_dword v180, v4, s[4:5] nt
	s_add_u32 s4, s4, 0x6000
	s_addc_u32 s5, s5, 0
	global_load_dword v182, v4, s[4:5] nt
	s_add_u32 s4, s4, 0x6000
	s_addc_u32 s5, s5, 0
	global_load_dword v184, v4, s[4:5] nt
	s_add_u32 s4, s4, 0x6000
	s_addc_u32 s5, s5, 0
	global_load_dword v186, v4, s[4:5] nt
	s_add_u32 s4, s4, 0x6000
	s_addc_u32 s5, s5, 0
	global_load_dword v188, v4, s[4:5] nt
	s_add_u32 s4, s4, 0x6000
	s_addc_u32 s5, s5, 0
	global_load_dword v190, v4, s[4:5] nt
	s_add_u32 s4, s4, 0x6000
	s_addc_u32 s5, s5, 0
	global_load_dword v192, v4, s[4:5] nt
	s_add_u32 s4, s4, 0x6000
	s_addc_u32 s5, s5, 0
	global_load_dword v194, v4, s[4:5] nt
	s_add_u32 s4, s4, 0x6000
	s_addc_u32 s5, s5, 0
	global_load_dword v196, v4, s[4:5] nt
	s_add_u32 s4, s4, 0x6000
	s_addc_u32 s5, s5, 0
	global_load_dword v198, v4, s[4:5] nt
	s_add_u32 s4, s4, 0x6000
	s_addc_u32 s5, s5, 0
	global_load_dword v200, v4, s[4:5] nt
	s_add_u32 s4, s4, 0x6000
	s_addc_u32 s5, s5, 0
	global_load_dword v202, v4, s[4:5] nt
	s_add_u32 s4, s4, 0x6000
	s_addc_u32 s5, s5, 0
	global_load_dword v204, v4, s[4:5] nt
	s_add_u32 s4, s4, 0x6000
	s_addc_u32 s5, s5, 0
	global_load_dword v206, v4, s[4:5] nt
	s_add_u32 s4, s4, 0x6000
	s_addc_u32 s5, s5, 0
	global_load_dword v208, v4, s[4:5] nt
	s_add_u32 s4, s4, 0x6000
	s_addc_u32 s5, s5, 0
	global_load_dword v210, v4, s[4:5] nt
	s_add_u32 s4, s4, 0x6000
	s_addc_u32 s5, s5, 0
	global_load_dword v212, v4, s[4:5] nt
	s_add_u32 s4, s4, 0x6000
	s_addc_u32 s5, s5, 0
	global_load_dword v214, v4, s[4:5] nt
	s_add_u32 s4, s4, 0x6000
	s_addc_u32 s5, s5, 0
	global_load_dword v216, v4, s[4:5] nt
	s_add_u32 s4, s4, 0x6000
	s_addc_u32 s5, s5, 0
	global_load_dword v218, v4, s[4:5] nt
	s_add_u32 s4, s4, 0x6000
	s_addc_u32 s5, s5, 0
	global_load_dword v220, v4, s[4:5] nt
	s_add_u32 s4, s4, 0x6000
	s_addc_u32 s5, s5, 0
	global_load_dword v222, v4, s[4:5] nt
	s_add_u32 s4, s4, 0x6000
	s_addc_u32 s5, s5, 0
	global_load_dword v224, v4, s[4:5] nt
	s_add_u32 s4, s4, 0x6000
	s_addc_u32 s5, s5, 0
	global_load_dword v226, v4, s[4:5] nt
	s_add_u32 s4, s4, 0x6000
	s_addc_u32 s5, s5, 0
	global_load_dword v228, v4, s[4:5] nt
	s_add_u32 s4, s4, 0x6000
	s_addc_u32 s5, s5, 0
	global_load_dword v230, v4, s[4:5] nt
	s_add_u32 s4, s4, 0x6000
	s_addc_u32 s5, s5, 0
	global_load_dword v232, v4, s[4:5] nt
	s_add_u32 s4, s4, 0x6000
	s_addc_u32 s5, s5, 0
	global_load_dword v234, v4, s[4:5] nt
	s_add_u32 s4, s4, 0x6000
	s_addc_u32 s5, s5, 0
	global_load_dword v236, v4, s[4:5] nt
	s_add_u32 s4, s4, 0x6000
	s_addc_u32 s5, s5, 0
	global_load_dword v238, v4, s[4:5] nt
	s_add_u32 s4, s4, 0x6000
	s_addc_u32 s5, s5, 0
	global_load_dword v240, v4, s[4:5] nt
	s_add_u32 s4, s4, 0x6000
	s_addc_u32 s5, s5, 0
	global_load_dword v242, v4, s[4:5] nt
	s_add_u32 s4, s4, 0x6000
	s_addc_u32 s5, s5, 0
	global_load_dword v244, v4, s[4:5] nt
	s_add_u32 s4, s4, 0x6000
	s_addc_u32 s5, s5, 0
	global_load_dword v246, v4, s[4:5] nt
	s_add_u32 s4, s4, 0x6000
	s_addc_u32 s5, s5, 0
	v_mov_b32_e32 v17, s11
	ds_read_b128 v[18:21], v17
	ds_read_b128 v[22:25], v17 offset:16
	ds_read_b128 v[26:29], v17 offset:4096
	ds_read_b128 v[30:33], v17 offset:4112
	ds_read_b128 v[36:39], v17 offset:8192
	ds_read_b128 v[40:43], v17 offset:8208
	ds_read_b128 v[44:47], v17 offset:12288
	ds_read_b128 v[48:51], v17 offset:12304
	ds_read_b128 v[52:55], v17 offset:16384
	ds_read_b128 v[56:59], v17 offset:16400
	ds_read_b128 v[60:63], v17 offset:20480
	ds_read_b128 v[64:67], v17 offset:20496
	ds_read_b128 v[68:71], v17 offset:24576
	ds_read_b128 v[72:75], v17 offset:24592
	ds_read_b128 v[76:79], v17 offset:28672
	ds_read_b128 v[80:83], v17 offset:28688
	s_add_i32 s11, s11, 32
	ds_read_b128 v[84:87], v17 offset:32768
	ds_read_b128 v[88:91], v17 offset:32784
	s_waitcnt lgkmcnt(0)
; #define GAS __attribute__((address_space(1)))
; #define NTLD(P) (NT_STREAMS ? __builtin_nontemporal_load(P) : *(P))
; __device__ __forceinline__ void p0_prologue(Frame& F) {
;     ...
; #pragma unroll 8
;             for (int kk = 0; kk < 128; ++kk) { const int k = F.wave * 128 + kk; const float w = NTLD((const GAS float*)(W + (size_t)k * 6144));
; #pragma unroll
;                 for (int r = 0; r < 9; ++r) a[r] += sc[r * 1024 + k] * w; }
	v_mov_b32_e32 v92, v18
	v_mov_b32_e32 v93, v26
	v_mov_b32_e32 v26, v19
	v_mov_b32_e32 v18, v20
	v_mov_b32_e32 v19, v28
	v_mov_b32_e32 v28, v21
	s_waitcnt lgkmcnt(13)
	v_mov_b32_e32 v20, v36
	s_waitcnt lgkmcnt(11)
	v_mov_b32_e32 v21, v44
	v_mov_b32_e32 v44, v37
	v_mov_b32_e32 v36, v38
	v_mov_b32_e32 v37, v46
	v_mov_b32_e32 v46, v39
	s_waitcnt lgkmcnt(9)
	v_mov_b32_e32 v38, v52
	s_waitcnt lgkmcnt(7)
	v_mov_b32_e32 v39, v60
	v_mov_b32_e32 v60, v53
	v_mov_b32_e32 v52, v54
	v_mov_b32_e32 v53, v62
	v_mov_b32_e32 v62, v55
	s_waitcnt lgkmcnt(5)
	v_mov_b32_e32 v54, v68
	s_waitcnt lgkmcnt(3)
	v_mov_b32_e32 v55, v76
	v_mov_b32_e32 v76, v69
	v_mov_b32_e32 v68, v70
	v_mov_b32_e32 v69, v78
	v_mov_b32_e32 v78, v71
	v_mov_b32_e32 v70, v22
	v_mov_b32_e32 v71, v30
	v_mov_b32_e32 v30, v23
	v_mov_b32_e32 v22, v24
	v_mov_b32_e32 v23, v32
	v_mov_b32_e32 v32, v25
	v_mov_b32_e32 v24, v40
	v_mov_b32_e32 v25, v48
	v_mov_b32_e32 v48, v41
	v_mov_b32_e32 v40, v42
	v_mov_b32_e32 v41, v50
	v_mov_b32_e32 v50, v43
	v_mov_b32_e32 v42, v56
	v_mov_b32_e32 v43, v64
	v_mov_b32_e32 v64, v57
	v_mov_b32_e32 v56, v58
	v_mov_b32_e32 v57, v66
	v_mov_b32_e32 v66, v59
	v_mov_b32_e32 v58, v72
	s_waitcnt lgkmcnt(2)
	v_mov_b32_e32 v59, v80
	v_mov_b32_e32 v80, v73
	v_mov_b32_e32 v72, v74
	v_mov_b32_e32 v73, v82
	v_mov_b32_e32 v82, v75
	s_waitcnt vmcnt(63)
	v_pk_fma_f32 v[8:9], v[120:121], v[92:93], v[8:9] op_sel_hi:[0,1,1]
	v_pk_fma_f32 v[10:11], v[120:121], v[20:21], v[10:11] op_sel_hi:[0,1,1]
	v_pk_fma_f32 v[12:13], v[120:121], v[38:39], v[12:13] op_sel_hi:[0,1,1]
	v_pk_fma_f32 v[14:15], v[120:121], v[54:55], v[14:15] op_sel_hi:[0,1,1]
	s_waitcnt lgkmcnt(1)
	v_fmac_f32_e32 v16, v120, v84
	s_waitcnt vmcnt(62)
	v_pk_fma_f32 v[8:9], v[122:123], v[26:27], v[8:9] op_sel_hi:[0,1,1]
	v_pk_fma_f32 v[10:11], v[122:123], v[44:45], v[10:11] op_sel_hi:[0,1,1]
	v_pk_fma_f32 v[12:13], v[122:123], v[60:61], v[12:13] op_sel_hi:[0,1,1]
	v_pk_fma_f32 v[14:15], v[122:123], v[76:77], v[14:15] op_sel_hi:[0,1,1]
	v_fmac_f32_e32 v16, v122, v85
	s_waitcnt vmcnt(61)
	v_pk_fma_f32 v[8:9], v[124:125], v[18:19], v[8:9] op_sel_hi:[0,1,1]
	v_pk_fma_f32 v[10:11], v[124:125], v[36:37], v[10:11] op_sel_hi:[0,1,1]
	v_pk_fma_f32 v[12:13], v[124:125], v[52:53], v[12:13] op_sel_hi:[0,1,1]
	v_pk_fma_f32 v[14:15], v[124:125], v[68:69], v[14:15] op_sel_hi:[0,1,1]
	v_fmac_f32_e32 v16, v124, v86
	s_waitcnt vmcnt(60)
	v_pk_fma_f32 v[8:9], v[126:127], v[28:29], v[8:9] op_sel_hi:[0,1,1]
	v_pk_fma_f32 v[10:11], v[126:127], v[46:47], v[10:11] op_sel_hi:[0,1,1]
	v_pk_fma_f32 v[12:13], v[126:127], v[62:63], v[12:13] op_sel_hi:[0,1,1]
	v_pk_fma_f32 v[14:15], v[126:127], v[78:79], v[14:15] op_sel_hi:[0,1,1]
	v_fmac_f32_e32 v16, v126, v87
	s_waitcnt vmcnt(59)
	v_pk_fma_f32 v[8:9], v[128:129], v[70:71], v[8:9] op_sel_hi:[0,1,1]
	v_pk_fma_f32 v[10:11], v[128:129], v[24:25], v[10:11] op_sel_hi:[0,1,1]
	v_pk_fma_f32 v[12:13], v[128:129], v[42:43], v[12:13] op_sel_hi:[0,1,1]
	v_pk_fma_f32 v[14:15], v[128:129], v[58:59], v[14:15] op_sel_hi:[0,1,1]
	s_waitcnt lgkmcnt(0)
	v_fmac_f32_e32 v16, v128, v88
	s_waitcnt vmcnt(58)
	v_pk_fma_f32 v[8:9], v[130:131], v[30:31], v[8:9] op_sel_hi:[0,1,1]
	v_pk_fma_f32 v[10:11], v[130:131], v[48:49], v[10:11] op_sel_hi:[0,1,1]
	v_pk_fma_f32 v[12:13], v[130:131], v[64:65], v[12:13] op_sel_hi:[0,1,1]
	v_pk_fma_f32 v[14:15], v[130:131], v[80:81], v[14:15] op_sel_hi:[0,1,1]
	v_fmac_f32_e32 v16, v130, v89
	s_waitcnt vmcnt(57)
	v_pk_fma_f32 v[8:9], v[132:133], v[22:23], v[8:9] op_sel_hi:[0,1,1]
	v_pk_fma_f32 v[10:11], v[132:133], v[40:41], v[10:11] op_sel_hi:[0,1,1]
	v_pk_fma_f32 v[12:13], v[132:133], v[56:57], v[12:13] op_sel_hi:[0,1,1]
	v_pk_fma_f32 v[14:15], v[132:133], v[72:73], v[14:15] op_sel_hi:[0,1,1]
	v_fmac_f32_e32 v16, v132, v90
	s_waitcnt vmcnt(56)
	v_pk_fma_f32 v[8:9], v[134:135], v[32:33], v[8:9] op_sel_hi:[0,1,1]
	v_pk_fma_f32 v[10:11], v[134:135], v[50:51], v[10:11] op_sel_hi:[0,1,1]
	v_pk_fma_f32 v[12:13], v[134:135], v[66:67], v[12:13] op_sel_hi:[0,1,1]
	v_pk_fma_f32 v[14:15], v[134:135], v[82:83], v[14:15] op_sel_hi:[0,1,1]
	v_fmac_f32_e32 v16, v134, v91
	v_mov_b32_e32 v17, s11
	ds_read_b128 v[18:21], v17
	ds_read_b128 v[22:25], v17 offset:16
	ds_read_b128 v[26:29], v17 offset:4096
	ds_read_b128 v[30:33], v17 offset:4112
	ds_read_b128 v[36:39], v17 offset:8192
	ds_read_b128 v[40:43], v17 offset:8208
	ds_read_b128 v[44:47], v17 offset:12288
	ds_read_b128 v[48:51], v17 offset:12304
	ds_read_b128 v[52:55], v17 offset:16384
	ds_read_b128 v[56:59], v17 offset:16400
	ds_read_b128 v[60:63], v17 offset:20480
	ds_read_b128 v[64:67], v17 offset:20496
	ds_read_b128 v[68:71], v17 offset:24576
	ds_read_b128 v[72:75], v17 offset:24592
	ds_read_b128 v[76:79], v17 offset:28672
	ds_read_b128 v[80:83], v17 offset:28688
	s_add_i32 s11, s11, 32
	ds_read_b128 v[84:87], v17 offset:32768
	ds_read_b128 v[88:91], v17 offset:32784
	s_waitcnt lgkmcnt(0)
	v_mov_b32_e32 v92, v18
	v_mov_b32_e32 v93, v26
	v_mov_b32_e32 v26, v19
	v_mov_b32_e32 v18, v20
	v_mov_b32_e32 v19, v28
	v_mov_b32_e32 v28, v21
	s_waitcnt lgkmcnt(13)
	v_mov_b32_e32 v20, v36
	s_waitcnt lgkmcnt(11)
	v_mov_b32_e32 v21, v44
	v_mov_b32_e32 v44, v37
	v_mov_b32_e32 v36, v38
	v_mov_b32_e32 v37, v46
	v_mov_b32_e32 v46, v39
	s_waitcnt lgkmcnt(9)
	v_mov_b32_e32 v38, v52
	s_waitcnt lgkmcnt(7)
	v_mov_b32_e32 v39, v60
	v_mov_b32_e32 v60, v53
	v_mov_b32_e32 v52, v54
	v_mov_b32_e32 v53, v62
	v_mov_b32_e32 v62, v55
	s_waitcnt lgkmcnt(5)
	v_mov_b32_e32 v54, v68
	s_waitcnt lgkmcnt(3)
; #define GAS __attribute__((address_space(1)))
; #define NTLD(P) (NT_STREAMS ? __builtin_nontemporal_load(P) : *(P))
; __device__ __forceinline__ void p0_prologue(Frame& F) {
;     ...
; #pragma unroll 8
;             for (int kk = 0; kk < 128; ++kk) { const int k = F.wave * 128 + kk; const float w = NTLD((const GAS float*)(W + (size_t)k * 6144));
; #pragma unroll
;                 for (int r = 0; r < 9; ++r) a[r] += sc[r * 1024 + k] * w; }
	v_mov_b32_e32 v55, v76
	v_mov_b32_e32 v76, v69
	v_mov_b32_e32 v68, v70
	v_mov_b32_e32 v69, v78
	v_mov_b32_e32 v78, v71
	v_mov_b32_e32 v70, v22
	v_mov_b32_e32 v71, v30
	v_mov_b32_e32 v30, v23
	v_mov_b32_e32 v22, v24
	v_mov_b32_e32 v23, v32
	v_mov_b32_e32 v32, v25
	v_mov_b32_e32 v24, v40
	v_mov_b32_e32 v25, v48
	v_mov_b32_e32 v48, v41
	v_mov_b32_e32 v40, v42
	v_mov_b32_e32 v41, v50
	v_mov_b32_e32 v50, v43
	v_mov_b32_e32 v42, v56
	v_mov_b32_e32 v43, v64
	v_mov_b32_e32 v64, v57
	v_mov_b32_e32 v56, v58
	v_mov_b32_e32 v57, v66
	v_mov_b32_e32 v66, v59
	v_mov_b32_e32 v58, v72
	s_waitcnt lgkmcnt(2)
	v_mov_b32_e32 v59, v80
	v_mov_b32_e32 v80, v73
	v_mov_b32_e32 v72, v74
	v_mov_b32_e32 v73, v82
	v_mov_b32_e32 v82, v75
	s_waitcnt vmcnt(55)
	v_pk_fma_f32 v[8:9], v[136:137], v[92:93], v[8:9] op_sel_hi:[0,1,1]
	v_pk_fma_f32 v[10:11], v[136:137], v[20:21], v[10:11] op_sel_hi:[0,1,1]
	v_pk_fma_f32 v[12:13], v[136:137], v[38:39], v[12:13] op_sel_hi:[0,1,1]
	v_pk_fma_f32 v[14:15], v[136:137], v[54:55], v[14:15] op_sel_hi:[0,1,1]
	s_waitcnt lgkmcnt(1)
	v_fmac_f32_e32 v16, v136, v84
	s_waitcnt vmcnt(54)
	v_pk_fma_f32 v[8:9], v[138:139], v[26:27], v[8:9] op_sel_hi:[0,1,1]
	v_pk_fma_f32 v[10:11], v[138:139], v[44:45], v[10:11] op_sel_hi:[0,1,1]
	v_pk_fma_f32 v[12:13], v[138:139], v[60:61], v[12:13] op_sel_hi:[0,1,1]
	v_pk_fma_f32 v[14:15], v[138:139], v[76:77], v[14:15] op_sel_hi:[0,1,1]
	v_fmac_f32_e32 v16, v138, v85
	s_waitcnt vmcnt(53)
	v_pk_fma_f32 v[8:9], v[140:141], v[18:19], v[8:9] op_sel_hi:[0,1,1]
	v_pk_fma_f32 v[10:11], v[140:141], v[36:37], v[10:11] op_sel_hi:[0,1,1]
	v_pk_fma_f32 v[12:13], v[140:141], v[52:53], v[12:13] op_sel_hi:[0,1,1]
	v_pk_fma_f32 v[14:15], v[140:141], v[68:69], v[14:15] op_sel_hi:[0,1,1]
	v_fmac_f32_e32 v16, v140, v86
	s_waitcnt vmcnt(52)
	v_pk_fma_f32 v[8:9], v[142:143], v[28:29], v[8:9] op_sel_hi:[0,1,1]
	v_pk_fma_f32 v[10:11], v[142:143], v[46:47], v[10:11] op_sel_hi:[0,1,1]
	v_pk_fma_f32 v[12:13], v[142:143], v[62:63], v[12:13] op_sel_hi:[0,1,1]
	v_pk_fma_f32 v[14:15], v[142:143], v[78:79], v[14:15] op_sel_hi:[0,1,1]
	v_fmac_f32_e32 v16, v142, v87
	s_waitcnt vmcnt(51)
	v_pk_fma_f32 v[8:9], v[144:145], v[70:71], v[8:9] op_sel_hi:[0,1,1]
	v_pk_fma_f32 v[10:11], v[144:145], v[24:25], v[10:11] op_sel_hi:[0,1,1]
	v_pk_fma_f32 v[12:13], v[144:145], v[42:43], v[12:13] op_sel_hi:[0,1,1]
	v_pk_fma_f32 v[14:15], v[144:145], v[58:59], v[14:15] op_sel_hi:[0,1,1]
	s_waitcnt lgkmcnt(0)
	v_fmac_f32_e32 v16, v144, v88
	s_waitcnt vmcnt(50)
	v_pk_fma_f32 v[8:9], v[146:147], v[30:31], v[8:9] op_sel_hi:[0,1,1]
	v_pk_fma_f32 v[10:11], v[146:147], v[48:49], v[10:11] op_sel_hi:[0,1,1]
	v_pk_fma_f32 v[12:13], v[146:147], v[64:65], v[12:13] op_sel_hi:[0,1,1]
	v_pk_fma_f32 v[14:15], v[146:147], v[80:81], v[14:15] op_sel_hi:[0,1,1]
	v_fmac_f32_e32 v16, v146, v89
	s_waitcnt vmcnt(49)
	v_pk_fma_f32 v[8:9], v[148:149], v[22:23], v[8:9] op_sel_hi:[0,1,1]
	v_pk_fma_f32 v[10:11], v[148:149], v[40:41], v[10:11] op_sel_hi:[0,1,1]
	v_pk_fma_f32 v[12:13], v[148:149], v[56:57], v[12:13] op_sel_hi:[0,1,1]
	v_pk_fma_f32 v[14:15], v[148:149], v[72:73], v[14:15] op_sel_hi:[0,1,1]
	v_fmac_f32_e32 v16, v148, v90
	s_waitcnt vmcnt(48)
	v_pk_fma_f32 v[8:9], v[150:151], v[32:33], v[8:9] op_sel_hi:[0,1,1]
	v_pk_fma_f32 v[10:11], v[150:151], v[50:51], v[10:11] op_sel_hi:[0,1,1]
	v_pk_fma_f32 v[12:13], v[150:151], v[66:67], v[12:13] op_sel_hi:[0,1,1]
	v_pk_fma_f32 v[14:15], v[150:151], v[82:83], v[14:15] op_sel_hi:[0,1,1]
	v_fmac_f32_e32 v16, v150, v91
	v_mov_b32_e32 v17, s11
	ds_read_b128 v[18:21], v17
	ds_read_b128 v[22:25], v17 offset:16
	ds_read_b128 v[26:29], v17 offset:4096
	ds_read_b128 v[30:33], v17 offset:4112
	ds_read_b128 v[36:39], v17 offset:8192
	ds_read_b128 v[40:43], v17 offset:8208
	ds_read_b128 v[44:47], v17 offset:12288
	ds_read_b128 v[48:51], v17 offset:12304
	ds_read_b128 v[52:55], v17 offset:16384
	ds_read_b128 v[56:59], v17 offset:16400
	ds_read_b128 v[60:63], v17 offset:20480
	ds_read_b128 v[64:67], v17 offset:20496
	ds_read_b128 v[68:71], v17 offset:24576
	ds_read_b128 v[72:75], v17 offset:24592
	ds_read_b128 v[76:79], v17 offset:28672
	ds_read_b128 v[80:83], v17 offset:28688
	s_add_i32 s11, s11, 32
	ds_read_b128 v[84:87], v17 offset:32768
	ds_read_b128 v[88:91], v17 offset:32784
	s_waitcnt lgkmcnt(0)
	v_mov_b32_e32 v92, v18
	v_mov_b32_e32 v93, v26
	v_mov_b32_e32 v26, v19
	v_mov_b32_e32 v18, v20
	v_mov_b32_e32 v19, v28
	v_mov_b32_e32 v28, v21
	s_waitcnt lgkmcnt(13)
	v_mov_b32_e32 v20, v36
	s_waitcnt lgkmcnt(11)
	v_mov_b32_e32 v21, v44
	v_mov_b32_e32 v44, v37
	v_mov_b32_e32 v36, v38
	v_mov_b32_e32 v37, v46
	v_mov_b32_e32 v46, v39
	s_waitcnt lgkmcnt(9)
	v_mov_b32_e32 v38, v52
	s_waitcnt lgkmcnt(7)
	v_mov_b32_e32 v39, v60
	v_mov_b32_e32 v60, v53
	v_mov_b32_e32 v52, v54
	v_mov_b32_e32 v53, v62
	v_mov_b32_e32 v62, v55
	s_waitcnt lgkmcnt(5)
	v_mov_b32_e32 v54, v68
	s_waitcnt lgkmcnt(3)
	v_mov_b32_e32 v55, v76
	v_mov_b32_e32 v76, v69
	v_mov_b32_e32 v68, v70
	v_mov_b32_e32 v69, v78
	v_mov_b32_e32 v78, v71
	v_mov_b32_e32 v70, v22
	v_mov_b32_e32 v71, v30
	v_mov_b32_e32 v30, v23
	v_mov_b32_e32 v22, v24
	v_mov_b32_e32 v23, v32
	v_mov_b32_e32 v32, v25
	v_mov_b32_e32 v24, v40
	v_mov_b32_e32 v25, v48
	v_mov_b32_e32 v48, v41
	v_mov_b32_e32 v40, v42
	v_mov_b32_e32 v41, v50
	v_mov_b32_e32 v50, v43
	v_mov_b32_e32 v42, v56
	v_mov_b32_e32 v43, v64
	v_mov_b32_e32 v64, v57
	v_mov_b32_e32 v56, v58
	v_mov_b32_e32 v57, v66
	v_mov_b32_e32 v66, v59
	v_mov_b32_e32 v58, v72
	s_waitcnt lgkmcnt(2)
	v_mov_b32_e32 v59, v80
	v_mov_b32_e32 v80, v73
	v_mov_b32_e32 v72, v74
	v_mov_b32_e32 v73, v82
	v_mov_b32_e32 v82, v75
	s_waitcnt vmcnt(47)
; #define GAS __attribute__((address_space(1)))
; #define NTLD(P) (NT_STREAMS ? __builtin_nontemporal_load(P) : *(P))
; __device__ __forceinline__ void p0_prologue(Frame& F) {
;     ...
; #pragma unroll 8
;             for (int kk = 0; kk < 128; ++kk) { const int k = F.wave * 128 + kk; const float w = NTLD((const GAS float*)(W + (size_t)k * 6144));
; #pragma unroll
;                 for (int r = 0; r < 9; ++r) a[r] += sc[r * 1024 + k] * w; }
	v_pk_fma_f32 v[8:9], v[152:153], v[92:93], v[8:9] op_sel_hi:[0,1,1]
	v_pk_fma_f32 v[10:11], v[152:153], v[20:21], v[10:11] op_sel_hi:[0,1,1]
	v_pk_fma_f32 v[12:13], v[152:153], v[38:39], v[12:13] op_sel_hi:[0,1,1]
	v_pk_fma_f32 v[14:15], v[152:153], v[54:55], v[14:15] op_sel_hi:[0,1,1]
	s_waitcnt lgkmcnt(1)
	v_fmac_f32_e32 v16, v152, v84
	s_waitcnt vmcnt(46)
	v_pk_fma_f32 v[8:9], v[154:155], v[26:27], v[8:9] op_sel_hi:[0,1,1]
	v_pk_fma_f32 v[10:11], v[154:155], v[44:45], v[10:11] op_sel_hi:[0,1,1]
	v_pk_fma_f32 v[12:13], v[154:155], v[60:61], v[12:13] op_sel_hi:[0,1,1]
	v_pk_fma_f32 v[14:15], v[154:155], v[76:77], v[14:15] op_sel_hi:[0,1,1]
	v_fmac_f32_e32 v16, v154, v85
	s_waitcnt vmcnt(45)
	v_pk_fma_f32 v[8:9], v[156:157], v[18:19], v[8:9] op_sel_hi:[0,1,1]
	v_pk_fma_f32 v[10:11], v[156:157], v[36:37], v[10:11] op_sel_hi:[0,1,1]
	v_pk_fma_f32 v[12:13], v[156:157], v[52:53], v[12:13] op_sel_hi:[0,1,1]
	v_pk_fma_f32 v[14:15], v[156:157], v[68:69], v[14:15] op_sel_hi:[0,1,1]
	v_fmac_f32_e32 v16, v156, v86
	s_waitcnt vmcnt(44)
	v_pk_fma_f32 v[8:9], v[158:159], v[28:29], v[8:9] op_sel_hi:[0,1,1]
	v_pk_fma_f32 v[10:11], v[158:159], v[46:47], v[10:11] op_sel_hi:[0,1,1]
	v_pk_fma_f32 v[12:13], v[158:159], v[62:63], v[12:13] op_sel_hi:[0,1,1]
	v_pk_fma_f32 v[14:15], v[158:159], v[78:79], v[14:15] op_sel_hi:[0,1,1]
	v_fmac_f32_e32 v16, v158, v87
	s_waitcnt vmcnt(43)
	v_pk_fma_f32 v[8:9], v[160:161], v[70:71], v[8:9] op_sel_hi:[0,1,1]
	v_pk_fma_f32 v[10:11], v[160:161], v[24:25], v[10:11] op_sel_hi:[0,1,1]
	v_pk_fma_f32 v[12:13], v[160:161], v[42:43], v[12:13] op_sel_hi:[0,1,1]
	v_pk_fma_f32 v[14:15], v[160:161], v[58:59], v[14:15] op_sel_hi:[0,1,1]
	s_waitcnt lgkmcnt(0)
	v_fmac_f32_e32 v16, v160, v88
	s_waitcnt vmcnt(42)
	v_pk_fma_f32 v[8:9], v[162:163], v[30:31], v[8:9] op_sel_hi:[0,1,1]
	v_pk_fma_f32 v[10:11], v[162:163], v[48:49], v[10:11] op_sel_hi:[0,1,1]
	v_pk_fma_f32 v[12:13], v[162:163], v[64:65], v[12:13] op_sel_hi:[0,1,1]
	v_pk_fma_f32 v[14:15], v[162:163], v[80:81], v[14:15] op_sel_hi:[0,1,1]
	v_fmac_f32_e32 v16, v162, v89
	s_waitcnt vmcnt(41)
	v_pk_fma_f32 v[8:9], v[164:165], v[22:23], v[8:9] op_sel_hi:[0,1,1]
	v_pk_fma_f32 v[10:11], v[164:165], v[40:41], v[10:11] op_sel_hi:[0,1,1]
	v_pk_fma_f32 v[12:13], v[164:165], v[56:57], v[12:13] op_sel_hi:[0,1,1]
	v_pk_fma_f32 v[14:15], v[164:165], v[72:73], v[14:15] op_sel_hi:[0,1,1]
	v_fmac_f32_e32 v16, v164, v90
	s_waitcnt vmcnt(40)
	v_pk_fma_f32 v[8:9], v[166:167], v[32:33], v[8:9] op_sel_hi:[0,1,1]
	v_pk_fma_f32 v[10:11], v[166:167], v[50:51], v[10:11] op_sel_hi:[0,1,1]
	v_pk_fma_f32 v[12:13], v[166:167], v[66:67], v[12:13] op_sel_hi:[0,1,1]
	v_pk_fma_f32 v[14:15], v[166:167], v[82:83], v[14:15] op_sel_hi:[0,1,1]
	v_fmac_f32_e32 v16, v166, v91
	v_mov_b32_e32 v17, s11
	ds_read_b128 v[18:21], v17
	ds_read_b128 v[22:25], v17 offset:16
	ds_read_b128 v[26:29], v17 offset:4096
	ds_read_b128 v[30:33], v17 offset:4112
	ds_read_b128 v[36:39], v17 offset:8192
	ds_read_b128 v[40:43], v17 offset:8208
	ds_read_b128 v[44:47], v17 offset:12288
	ds_read_b128 v[48:51], v17 offset:12304
	ds_read_b128 v[52:55], v17 offset:16384
	ds_read_b128 v[56:59], v17 offset:16400
	ds_read_b128 v[60:63], v17 offset:20480
	ds_read_b128 v[64:67], v17 offset:20496
	ds_read_b128 v[68:71], v17 offset:24576
	ds_read_b128 v[72:75], v17 offset:24592
	ds_read_b128 v[76:79], v17 offset:28672
	ds_read_b128 v[80:83], v17 offset:28688
	s_add_i32 s11, s11, 32
	ds_read_b128 v[84:87], v17 offset:32768
	ds_read_b128 v[88:91], v17 offset:32784
	s_waitcnt lgkmcnt(0)
	v_mov_b32_e32 v92, v18
	v_mov_b32_e32 v93, v26
	v_mov_b32_e32 v26, v19
	v_mov_b32_e32 v18, v20
	v_mov_b32_e32 v19, v28
	v_mov_b32_e32 v28, v21
	s_waitcnt lgkmcnt(13)
	v_mov_b32_e32 v20, v36
	s_waitcnt lgkmcnt(11)
	v_mov_b32_e32 v21, v44
	v_mov_b32_e32 v44, v37
	v_mov_b32_e32 v36, v38
	v_mov_b32_e32 v37, v46
	v_mov_b32_e32 v46, v39
	s_waitcnt lgkmcnt(9)
	v_mov_b32_e32 v38, v52
	s_waitcnt lgkmcnt(7)
	v_mov_b32_e32 v39, v60
	v_mov_b32_e32 v60, v53
	v_mov_b32_e32 v52, v54
	v_mov_b32_e32 v53, v62
	v_mov_b32_e32 v62, v55
	s_waitcnt lgkmcnt(5)
	v_mov_b32_e32 v54, v68
	s_waitcnt lgkmcnt(3)
	v_mov_b32_e32 v55, v76
	v_mov_b32_e32 v76, v69
	v_mov_b32_e32 v68, v70
	v_mov_b32_e32 v69, v78
	v_mov_b32_e32 v78, v71
	v_mov_b32_e32 v70, v22
	v_mov_b32_e32 v71, v30
	v_mov_b32_e32 v30, v23
	v_mov_b32_e32 v22, v24
	v_mov_b32_e32 v23, v32
	v_mov_b32_e32 v32, v25
	v_mov_b32_e32 v24, v40
	v_mov_b32_e32 v25, v48
	v_mov_b32_e32 v48, v41
	v_mov_b32_e32 v40, v42
	v_mov_b32_e32 v41, v50
	v_mov_b32_e32 v50, v43
	v_mov_b32_e32 v42, v56
	v_mov_b32_e32 v43, v64
	v_mov_b32_e32 v64, v57
	v_mov_b32_e32 v56, v58
	v_mov_b32_e32 v57, v66
	v_mov_b32_e32 v66, v59
	v_mov_b32_e32 v58, v72
	s_waitcnt lgkmcnt(2)
	v_mov_b32_e32 v59, v80
	v_mov_b32_e32 v80, v73
	v_mov_b32_e32 v72, v74
	v_mov_b32_e32 v73, v82
	v_mov_b32_e32 v82, v75
	s_waitcnt vmcnt(39)
	v_pk_fma_f32 v[8:9], v[168:169], v[92:93], v[8:9] op_sel_hi:[0,1,1]
	v_pk_fma_f32 v[10:11], v[168:169], v[20:21], v[10:11] op_sel_hi:[0,1,1]
	v_pk_fma_f32 v[12:13], v[168:169], v[38:39], v[12:13] op_sel_hi:[0,1,1]
	v_pk_fma_f32 v[14:15], v[168:169], v[54:55], v[14:15] op_sel_hi:[0,1,1]
	s_waitcnt lgkmcnt(1)
	v_fmac_f32_e32 v16, v168, v84
	s_waitcnt vmcnt(38)
	v_pk_fma_f32 v[8:9], v[170:171], v[26:27], v[8:9] op_sel_hi:[0,1,1]
	v_pk_fma_f32 v[10:11], v[170:171], v[44:45], v[10:11] op_sel_hi:[0,1,1]
	v_pk_fma_f32 v[12:13], v[170:171], v[60:61], v[12:13] op_sel_hi:[0,1,1]
	v_pk_fma_f32 v[14:15], v[170:171], v[76:77], v[14:15] op_sel_hi:[0,1,1]
	v_fmac_f32_e32 v16, v170, v85
	s_waitcnt vmcnt(37)
; #define GAS __attribute__((address_space(1)))
; #define NTLD(P) (NT_STREAMS ? __builtin_nontemporal_load(P) : *(P))
; __device__ __forceinline__ void p0_prologue(Frame& F) {
;     ...
; #pragma unroll 8
;             for (int kk = 0; kk < 128; ++kk) { const int k = F.wave * 128 + kk; const float w = NTLD((const GAS float*)(W + (size_t)k * 6144));
; #pragma unroll
;                 for (int r = 0; r < 9; ++r) a[r] += sc[r * 1024 + k] * w; }
	v_pk_fma_f32 v[8:9], v[172:173], v[18:19], v[8:9] op_sel_hi:[0,1,1]
	v_pk_fma_f32 v[10:11], v[172:173], v[36:37], v[10:11] op_sel_hi:[0,1,1]
	v_pk_fma_f32 v[12:13], v[172:173], v[52:53], v[12:13] op_sel_hi:[0,1,1]
	v_pk_fma_f32 v[14:15], v[172:173], v[68:69], v[14:15] op_sel_hi:[0,1,1]
	v_fmac_f32_e32 v16, v172, v86
	s_waitcnt vmcnt(36)
	v_pk_fma_f32 v[8:9], v[174:175], v[28:29], v[8:9] op_sel_hi:[0,1,1]
	v_pk_fma_f32 v[10:11], v[174:175], v[46:47], v[10:11] op_sel_hi:[0,1,1]
	v_pk_fma_f32 v[12:13], v[174:175], v[62:63], v[12:13] op_sel_hi:[0,1,1]
	v_pk_fma_f32 v[14:15], v[174:175], v[78:79], v[14:15] op_sel_hi:[0,1,1]
	v_fmac_f32_e32 v16, v174, v87
	s_waitcnt vmcnt(35)
	v_pk_fma_f32 v[8:9], v[176:177], v[70:71], v[8:9] op_sel_hi:[0,1,1]
	v_pk_fma_f32 v[10:11], v[176:177], v[24:25], v[10:11] op_sel_hi:[0,1,1]
	v_pk_fma_f32 v[12:13], v[176:177], v[42:43], v[12:13] op_sel_hi:[0,1,1]
	v_pk_fma_f32 v[14:15], v[176:177], v[58:59], v[14:15] op_sel_hi:[0,1,1]
	s_waitcnt lgkmcnt(0)
	v_fmac_f32_e32 v16, v176, v88
	s_waitcnt vmcnt(34)
	v_pk_fma_f32 v[8:9], v[178:179], v[30:31], v[8:9] op_sel_hi:[0,1,1]
	v_pk_fma_f32 v[10:11], v[178:179], v[48:49], v[10:11] op_sel_hi:[0,1,1]
	v_pk_fma_f32 v[12:13], v[178:179], v[64:65], v[12:13] op_sel_hi:[0,1,1]
	v_pk_fma_f32 v[14:15], v[178:179], v[80:81], v[14:15] op_sel_hi:[0,1,1]
	v_fmac_f32_e32 v16, v178, v89
	s_waitcnt vmcnt(33)
	v_pk_fma_f32 v[8:9], v[180:181], v[22:23], v[8:9] op_sel_hi:[0,1,1]
	v_pk_fma_f32 v[10:11], v[180:181], v[40:41], v[10:11] op_sel_hi:[0,1,1]
	v_pk_fma_f32 v[12:13], v[180:181], v[56:57], v[12:13] op_sel_hi:[0,1,1]
	v_pk_fma_f32 v[14:15], v[180:181], v[72:73], v[14:15] op_sel_hi:[0,1,1]
	v_fmac_f32_e32 v16, v180, v90
	s_waitcnt vmcnt(32)
	v_pk_fma_f32 v[8:9], v[182:183], v[32:33], v[8:9] op_sel_hi:[0,1,1]
	v_pk_fma_f32 v[10:11], v[182:183], v[50:51], v[10:11] op_sel_hi:[0,1,1]
	v_pk_fma_f32 v[12:13], v[182:183], v[66:67], v[12:13] op_sel_hi:[0,1,1]
	v_pk_fma_f32 v[14:15], v[182:183], v[82:83], v[14:15] op_sel_hi:[0,1,1]
	v_fmac_f32_e32 v16, v182, v91
	v_mov_b32_e32 v17, s11
	ds_read_b128 v[18:21], v17
	ds_read_b128 v[22:25], v17 offset:16
	ds_read_b128 v[26:29], v17 offset:4096
	ds_read_b128 v[30:33], v17 offset:4112
	ds_read_b128 v[36:39], v17 offset:8192
	ds_read_b128 v[40:43], v17 offset:8208
	ds_read_b128 v[44:47], v17 offset:12288
	ds_read_b128 v[48:51], v17 offset:12304
	ds_read_b128 v[52:55], v17 offset:16384
	ds_read_b128 v[56:59], v17 offset:16400
	ds_read_b128 v[60:63], v17 offset:20480
	ds_read_b128 v[64:67], v17 offset:20496
	ds_read_b128 v[68:71], v17 offset:24576
	ds_read_b128 v[72:75], v17 offset:24592
	ds_read_b128 v[76:79], v17 offset:28672
	ds_read_b128 v[80:83], v17 offset:28688
	s_add_i32 s11, s11, 32
	ds_read_b128 v[84:87], v17 offset:32768
	ds_read_b128 v[88:91], v17 offset:32784
	s_waitcnt lgkmcnt(0)
	v_mov_b32_e32 v92, v18
	v_mov_b32_e32 v93, v26
	v_mov_b32_e32 v26, v19
	v_mov_b32_e32 v18, v20
	v_mov_b32_e32 v19, v28
	v_mov_b32_e32 v28, v21
	s_waitcnt lgkmcnt(13)
	v_mov_b32_e32 v20, v36
	s_waitcnt lgkmcnt(11)
	v_mov_b32_e32 v21, v44
	v_mov_b32_e32 v44, v37
	v_mov_b32_e32 v36, v38
	v_mov_b32_e32 v37, v46
	v_mov_b32_e32 v46, v39
	s_waitcnt lgkmcnt(9)
	v_mov_b32_e32 v38, v52
	s_waitcnt lgkmcnt(7)
	v_mov_b32_e32 v39, v60
	v_mov_b32_e32 v60, v53
	v_mov_b32_e32 v52, v54
	v_mov_b32_e32 v53, v62
	v_mov_b32_e32 v62, v55
	s_waitcnt lgkmcnt(5)
	v_mov_b32_e32 v54, v68
	s_waitcnt lgkmcnt(3)
	v_mov_b32_e32 v55, v76
	v_mov_b32_e32 v76, v69
	v_mov_b32_e32 v68, v70
	v_mov_b32_e32 v69, v78
	v_mov_b32_e32 v78, v71
	v_mov_b32_e32 v70, v22
	v_mov_b32_e32 v71, v30
	v_mov_b32_e32 v30, v23
	v_mov_b32_e32 v22, v24
	v_mov_b32_e32 v23, v32
	v_mov_b32_e32 v32, v25
	v_mov_b32_e32 v24, v40
	v_mov_b32_e32 v25, v48
	v_mov_b32_e32 v48, v41
	v_mov_b32_e32 v40, v42
	v_mov_b32_e32 v41, v50
	v_mov_b32_e32 v50, v43
	v_mov_b32_e32 v42, v56
	v_mov_b32_e32 v43, v64
	v_mov_b32_e32 v64, v57
	v_mov_b32_e32 v56, v58
	v_mov_b32_e32 v57, v66
	v_mov_b32_e32 v66, v59
	v_mov_b32_e32 v58, v72
	s_waitcnt lgkmcnt(2)
	v_mov_b32_e32 v59, v80
	v_mov_b32_e32 v80, v73
	v_mov_b32_e32 v72, v74
	v_mov_b32_e32 v73, v82
	v_mov_b32_e32 v82, v75
	s_waitcnt vmcnt(31)
	v_pk_fma_f32 v[8:9], v[184:185], v[92:93], v[8:9] op_sel_hi:[0,1,1]
	v_pk_fma_f32 v[10:11], v[184:185], v[20:21], v[10:11] op_sel_hi:[0,1,1]
	v_pk_fma_f32 v[12:13], v[184:185], v[38:39], v[12:13] op_sel_hi:[0,1,1]
	v_pk_fma_f32 v[14:15], v[184:185], v[54:55], v[14:15] op_sel_hi:[0,1,1]
	s_waitcnt lgkmcnt(1)
	v_fmac_f32_e32 v16, v184, v84
	s_waitcnt vmcnt(30)
	v_pk_fma_f32 v[8:9], v[186:187], v[26:27], v[8:9] op_sel_hi:[0,1,1]
	v_pk_fma_f32 v[10:11], v[186:187], v[44:45], v[10:11] op_sel_hi:[0,1,1]
	v_pk_fma_f32 v[12:13], v[186:187], v[60:61], v[12:13] op_sel_hi:[0,1,1]
	v_pk_fma_f32 v[14:15], v[186:187], v[76:77], v[14:15] op_sel_hi:[0,1,1]
	v_fmac_f32_e32 v16, v186, v85
	s_waitcnt vmcnt(29)
	v_pk_fma_f32 v[8:9], v[188:189], v[18:19], v[8:9] op_sel_hi:[0,1,1]
	v_pk_fma_f32 v[10:11], v[188:189], v[36:37], v[10:11] op_sel_hi:[0,1,1]
	v_pk_fma_f32 v[12:13], v[188:189], v[52:53], v[12:13] op_sel_hi:[0,1,1]
	v_pk_fma_f32 v[14:15], v[188:189], v[68:69], v[14:15] op_sel_hi:[0,1,1]
	v_fmac_f32_e32 v16, v188, v86
	s_waitcnt vmcnt(28)
	v_pk_fma_f32 v[8:9], v[190:191], v[28:29], v[8:9] op_sel_hi:[0,1,1]
	v_pk_fma_f32 v[10:11], v[190:191], v[46:47], v[10:11] op_sel_hi:[0,1,1]
	v_pk_fma_f32 v[12:13], v[190:191], v[62:63], v[12:13] op_sel_hi:[0,1,1]
	v_pk_fma_f32 v[14:15], v[190:191], v[78:79], v[14:15] op_sel_hi:[0,1,1]
	v_fmac_f32_e32 v16, v190, v87
	s_waitcnt vmcnt(27)
; #define GAS __attribute__((address_space(1)))
; #define NTLD(P) (NT_STREAMS ? __builtin_nontemporal_load(P) : *(P))
; __device__ __forceinline__ void p0_prologue(Frame& F) {
;     ...
; #pragma unroll 8
;             for (int kk = 0; kk < 128; ++kk) { const int k = F.wave * 128 + kk; const float w = NTLD((const GAS float*)(W + (size_t)k * 6144));
; #pragma unroll
;                 for (int r = 0; r < 9; ++r) a[r] += sc[r * 1024 + k] * w; }
	v_pk_fma_f32 v[8:9], v[192:193], v[70:71], v[8:9] op_sel_hi:[0,1,1]
	v_pk_fma_f32 v[10:11], v[192:193], v[24:25], v[10:11] op_sel_hi:[0,1,1]
	v_pk_fma_f32 v[12:13], v[192:193], v[42:43], v[12:13] op_sel_hi:[0,1,1]
	v_pk_fma_f32 v[14:15], v[192:193], v[58:59], v[14:15] op_sel_hi:[0,1,1]
	s_waitcnt lgkmcnt(0)
	v_fmac_f32_e32 v16, v192, v88
	s_waitcnt vmcnt(26)
	v_pk_fma_f32 v[8:9], v[194:195], v[30:31], v[8:9] op_sel_hi:[0,1,1]
	v_pk_fma_f32 v[10:11], v[194:195], v[48:49], v[10:11] op_sel_hi:[0,1,1]
	v_pk_fma_f32 v[12:13], v[194:195], v[64:65], v[12:13] op_sel_hi:[0,1,1]
	v_pk_fma_f32 v[14:15], v[194:195], v[80:81], v[14:15] op_sel_hi:[0,1,1]
	v_fmac_f32_e32 v16, v194, v89
	s_waitcnt vmcnt(25)
	v_pk_fma_f32 v[8:9], v[196:197], v[22:23], v[8:9] op_sel_hi:[0,1,1]
	v_pk_fma_f32 v[10:11], v[196:197], v[40:41], v[10:11] op_sel_hi:[0,1,1]
	v_pk_fma_f32 v[12:13], v[196:197], v[56:57], v[12:13] op_sel_hi:[0,1,1]
	v_pk_fma_f32 v[14:15], v[196:197], v[72:73], v[14:15] op_sel_hi:[0,1,1]
	v_fmac_f32_e32 v16, v196, v90
	s_waitcnt vmcnt(24)
	v_pk_fma_f32 v[8:9], v[198:199], v[32:33], v[8:9] op_sel_hi:[0,1,1]
	v_pk_fma_f32 v[10:11], v[198:199], v[50:51], v[10:11] op_sel_hi:[0,1,1]
	v_pk_fma_f32 v[12:13], v[198:199], v[66:67], v[12:13] op_sel_hi:[0,1,1]
	v_pk_fma_f32 v[14:15], v[198:199], v[82:83], v[14:15] op_sel_hi:[0,1,1]
	v_fmac_f32_e32 v16, v198, v91
	v_mov_b32_e32 v17, s11
	ds_read_b128 v[18:21], v17
	ds_read_b128 v[22:25], v17 offset:16
	ds_read_b128 v[26:29], v17 offset:4096
	ds_read_b128 v[30:33], v17 offset:4112
	ds_read_b128 v[36:39], v17 offset:8192
	ds_read_b128 v[40:43], v17 offset:8208
	ds_read_b128 v[44:47], v17 offset:12288
	ds_read_b128 v[48:51], v17 offset:12304
	ds_read_b128 v[52:55], v17 offset:16384
	ds_read_b128 v[56:59], v17 offset:16400
	ds_read_b128 v[60:63], v17 offset:20480
	ds_read_b128 v[64:67], v17 offset:20496
	ds_read_b128 v[68:71], v17 offset:24576
	ds_read_b128 v[72:75], v17 offset:24592
	ds_read_b128 v[76:79], v17 offset:28672
	ds_read_b128 v[80:83], v17 offset:28688
	s_add_i32 s11, s11, 32
	ds_read_b128 v[84:87], v17 offset:32768
	ds_read_b128 v[88:91], v17 offset:32784
	s_waitcnt lgkmcnt(0)
	v_mov_b32_e32 v92, v18
	v_mov_b32_e32 v93, v26
	v_mov_b32_e32 v26, v19
	v_mov_b32_e32 v18, v20
	v_mov_b32_e32 v19, v28
	v_mov_b32_e32 v28, v21
	s_waitcnt lgkmcnt(13)
	v_mov_b32_e32 v20, v36
	s_waitcnt lgkmcnt(11)
	v_mov_b32_e32 v21, v44
	v_mov_b32_e32 v44, v37
	v_mov_b32_e32 v36, v38
	v_mov_b32_e32 v37, v46
	v_mov_b32_e32 v46, v39
	s_waitcnt lgkmcnt(9)
	v_mov_b32_e32 v38, v52
	s_waitcnt lgkmcnt(7)
	v_mov_b32_e32 v39, v60
	v_mov_b32_e32 v60, v53
	v_mov_b32_e32 v52, v54
	v_mov_b32_e32 v53, v62
	v_mov_b32_e32 v62, v55
	s_waitcnt lgkmcnt(5)
	v_mov_b32_e32 v54, v68
	s_waitcnt lgkmcnt(3)
	v_mov_b32_e32 v55, v76
	v_mov_b32_e32 v76, v69
	v_mov_b32_e32 v68, v70
	v_mov_b32_e32 v69, v78
	v_mov_b32_e32 v78, v71
	v_mov_b32_e32 v70, v22
	v_mov_b32_e32 v71, v30
	v_mov_b32_e32 v30, v23
	v_mov_b32_e32 v22, v24
	v_mov_b32_e32 v23, v32
	v_mov_b32_e32 v32, v25
	v_mov_b32_e32 v24, v40
	v_mov_b32_e32 v25, v48
	v_mov_b32_e32 v48, v41
	v_mov_b32_e32 v40, v42
	v_mov_b32_e32 v41, v50
	v_mov_b32_e32 v50, v43
	v_mov_b32_e32 v42, v56
	v_mov_b32_e32 v43, v64
	v_mov_b32_e32 v64, v57
	v_mov_b32_e32 v56, v58
	v_mov_b32_e32 v57, v66
	v_mov_b32_e32 v66, v59
	v_mov_b32_e32 v58, v72
	s_waitcnt lgkmcnt(2)
	v_mov_b32_e32 v59, v80
	v_mov_b32_e32 v80, v73
	v_mov_b32_e32 v72, v74
	v_mov_b32_e32 v73, v82
	v_mov_b32_e32 v82, v75
	s_waitcnt vmcnt(23)
	v_pk_fma_f32 v[8:9], v[200:201], v[92:93], v[8:9] op_sel_hi:[0,1,1]
	v_pk_fma_f32 v[10:11], v[200:201], v[20:21], v[10:11] op_sel_hi:[0,1,1]
	v_pk_fma_f32 v[12:13], v[200:201], v[38:39], v[12:13] op_sel_hi:[0,1,1]
	v_pk_fma_f32 v[14:15], v[200:201], v[54:55], v[14:15] op_sel_hi:[0,1,1]
	s_waitcnt lgkmcnt(1)
	v_fmac_f32_e32 v16, v200, v84
	s_waitcnt vmcnt(22)
	v_pk_fma_f32 v[8:9], v[202:203], v[26:27], v[8:9] op_sel_hi:[0,1,1]
	v_pk_fma_f32 v[10:11], v[202:203], v[44:45], v[10:11] op_sel_hi:[0,1,1]
	v_pk_fma_f32 v[12:13], v[202:203], v[60:61], v[12:13] op_sel_hi:[0,1,1]
	v_pk_fma_f32 v[14:15], v[202:203], v[76:77], v[14:15] op_sel_hi:[0,1,1]
	v_fmac_f32_e32 v16, v202, v85
	s_waitcnt vmcnt(21)
	v_pk_fma_f32 v[8:9], v[204:205], v[18:19], v[8:9] op_sel_hi:[0,1,1]
	v_pk_fma_f32 v[10:11], v[204:205], v[36:37], v[10:11] op_sel_hi:[0,1,1]
	v_pk_fma_f32 v[12:13], v[204:205], v[52:53], v[12:13] op_sel_hi:[0,1,1]
	v_pk_fma_f32 v[14:15], v[204:205], v[68:69], v[14:15] op_sel_hi:[0,1,1]
	v_fmac_f32_e32 v16, v204, v86
	s_waitcnt vmcnt(20)
	v_pk_fma_f32 v[8:9], v[206:207], v[28:29], v[8:9] op_sel_hi:[0,1,1]
	v_pk_fma_f32 v[10:11], v[206:207], v[46:47], v[10:11] op_sel_hi:[0,1,1]
	v_pk_fma_f32 v[12:13], v[206:207], v[62:63], v[12:13] op_sel_hi:[0,1,1]
	v_pk_fma_f32 v[14:15], v[206:207], v[78:79], v[14:15] op_sel_hi:[0,1,1]
	v_fmac_f32_e32 v16, v206, v87
	s_waitcnt vmcnt(19)
	v_pk_fma_f32 v[8:9], v[208:209], v[70:71], v[8:9] op_sel_hi:[0,1,1]
	v_pk_fma_f32 v[10:11], v[208:209], v[24:25], v[10:11] op_sel_hi:[0,1,1]
	v_pk_fma_f32 v[12:13], v[208:209], v[42:43], v[12:13] op_sel_hi:[0,1,1]
	v_pk_fma_f32 v[14:15], v[208:209], v[58:59], v[14:15] op_sel_hi:[0,1,1]
	s_waitcnt lgkmcnt(0)
	v_fmac_f32_e32 v16, v208, v88
	s_waitcnt vmcnt(18)
	v_pk_fma_f32 v[8:9], v[210:211], v[30:31], v[8:9] op_sel_hi:[0,1,1]
	v_pk_fma_f32 v[10:11], v[210:211], v[48:49], v[10:11] op_sel_hi:[0,1,1]
	v_pk_fma_f32 v[12:13], v[210:211], v[64:65], v[12:13] op_sel_hi:[0,1,1]
	v_pk_fma_f32 v[14:15], v[210:211], v[80:81], v[14:15] op_sel_hi:[0,1,1]
	v_fmac_f32_e32 v16, v210, v89
	s_waitcnt vmcnt(17)
; #define GAS __attribute__((address_space(1)))
; #define NTLD(P) (NT_STREAMS ? __builtin_nontemporal_load(P) : *(P))
; __device__ __forceinline__ void p0_prologue(Frame& F) {
;     ...
; #pragma unroll 8
;             for (int kk = 0; kk < 128; ++kk) { const int k = F.wave * 128 + kk; const float w = NTLD((const GAS float*)(W + (size_t)k * 6144));
; #pragma unroll
;                 for (int r = 0; r < 9; ++r) a[r] += sc[r * 1024 + k] * w; }
	v_pk_fma_f32 v[8:9], v[212:213], v[22:23], v[8:9] op_sel_hi:[0,1,1]
	v_pk_fma_f32 v[10:11], v[212:213], v[40:41], v[10:11] op_sel_hi:[0,1,1]
	v_pk_fma_f32 v[12:13], v[212:213], v[56:57], v[12:13] op_sel_hi:[0,1,1]
	v_pk_fma_f32 v[14:15], v[212:213], v[72:73], v[14:15] op_sel_hi:[0,1,1]
	v_fmac_f32_e32 v16, v212, v90
	s_waitcnt vmcnt(16)
	v_pk_fma_f32 v[8:9], v[214:215], v[32:33], v[8:9] op_sel_hi:[0,1,1]
	v_pk_fma_f32 v[10:11], v[214:215], v[50:51], v[10:11] op_sel_hi:[0,1,1]
	v_pk_fma_f32 v[12:13], v[214:215], v[66:67], v[12:13] op_sel_hi:[0,1,1]
	v_pk_fma_f32 v[14:15], v[214:215], v[82:83], v[14:15] op_sel_hi:[0,1,1]
	v_fmac_f32_e32 v16, v214, v91
	v_mov_b32_e32 v17, s11
	ds_read_b128 v[18:21], v17
	ds_read_b128 v[22:25], v17 offset:16
	ds_read_b128 v[26:29], v17 offset:4096
	ds_read_b128 v[30:33], v17 offset:4112
	ds_read_b128 v[36:39], v17 offset:8192
	ds_read_b128 v[40:43], v17 offset:8208
	ds_read_b128 v[44:47], v17 offset:12288
	ds_read_b128 v[48:51], v17 offset:12304
	ds_read_b128 v[52:55], v17 offset:16384
	ds_read_b128 v[56:59], v17 offset:16400
	ds_read_b128 v[60:63], v17 offset:20480
	ds_read_b128 v[64:67], v17 offset:20496
	ds_read_b128 v[68:71], v17 offset:24576
	ds_read_b128 v[72:75], v17 offset:24592
	ds_read_b128 v[76:79], v17 offset:28672
	ds_read_b128 v[80:83], v17 offset:28688
	s_add_i32 s11, s11, 32
	ds_read_b128 v[84:87], v17 offset:32768
	ds_read_b128 v[88:91], v17 offset:32784
	s_waitcnt lgkmcnt(0)
	v_mov_b32_e32 v92, v18
	v_mov_b32_e32 v93, v26
	v_mov_b32_e32 v26, v19
	v_mov_b32_e32 v18, v20
	v_mov_b32_e32 v19, v28
	v_mov_b32_e32 v28, v21
	s_waitcnt lgkmcnt(13)
	v_mov_b32_e32 v20, v36
	s_waitcnt lgkmcnt(11)
	v_mov_b32_e32 v21, v44
	v_mov_b32_e32 v44, v37
	v_mov_b32_e32 v36, v38
	v_mov_b32_e32 v37, v46
	v_mov_b32_e32 v46, v39
	s_waitcnt lgkmcnt(9)
	v_mov_b32_e32 v38, v52
	s_waitcnt lgkmcnt(7)
	v_mov_b32_e32 v39, v60
	v_mov_b32_e32 v60, v53
	v_mov_b32_e32 v52, v54
	v_mov_b32_e32 v53, v62
	v_mov_b32_e32 v62, v55
	s_waitcnt lgkmcnt(5)
	v_mov_b32_e32 v54, v68
	s_waitcnt lgkmcnt(3)
	v_mov_b32_e32 v55, v76
	v_mov_b32_e32 v76, v69
	v_mov_b32_e32 v68, v70
	v_mov_b32_e32 v69, v78
	v_mov_b32_e32 v78, v71
	v_mov_b32_e32 v70, v22
	v_mov_b32_e32 v71, v30
	v_mov_b32_e32 v30, v23
	v_mov_b32_e32 v22, v24
	v_mov_b32_e32 v23, v32
	v_mov_b32_e32 v32, v25
	v_mov_b32_e32 v24, v40
	v_mov_b32_e32 v25, v48
	v_mov_b32_e32 v48, v41
	v_mov_b32_e32 v40, v42
	v_mov_b32_e32 v41, v50
	v_mov_b32_e32 v50, v43
	v_mov_b32_e32 v42, v56
	v_mov_b32_e32 v43, v64
	v_mov_b32_e32 v64, v57
	v_mov_b32_e32 v56, v58
	v_mov_b32_e32 v57, v66
	v_mov_b32_e32 v66, v59
	v_mov_b32_e32 v58, v72
	s_waitcnt lgkmcnt(2)
	v_mov_b32_e32 v59, v80
	v_mov_b32_e32 v80, v73
	v_mov_b32_e32 v72, v74
	v_mov_b32_e32 v73, v82
	v_mov_b32_e32 v82, v75
	s_waitcnt vmcnt(15)
	v_pk_fma_f32 v[8:9], v[216:217], v[92:93], v[8:9] op_sel_hi:[0,1,1]
	v_pk_fma_f32 v[10:11], v[216:217], v[20:21], v[10:11] op_sel_hi:[0,1,1]
	v_pk_fma_f32 v[12:13], v[216:217], v[38:39], v[12:13] op_sel_hi:[0,1,1]
	v_pk_fma_f32 v[14:15], v[216:217], v[54:55], v[14:15] op_sel_hi:[0,1,1]
	s_waitcnt lgkmcnt(1)
	v_fmac_f32_e32 v16, v216, v84
	s_waitcnt vmcnt(14)
	v_pk_fma_f32 v[8:9], v[218:219], v[26:27], v[8:9] op_sel_hi:[0,1,1]
	v_pk_fma_f32 v[10:11], v[218:219], v[44:45], v[10:11] op_sel_hi:[0,1,1]
	v_pk_fma_f32 v[12:13], v[218:219], v[60:61], v[12:13] op_sel_hi:[0,1,1]
	v_pk_fma_f32 v[14:15], v[218:219], v[76:77], v[14:15] op_sel_hi:[0,1,1]
	v_fmac_f32_e32 v16, v218, v85
	s_waitcnt vmcnt(13)
	v_pk_fma_f32 v[8:9], v[220:221], v[18:19], v[8:9] op_sel_hi:[0,1,1]
	v_pk_fma_f32 v[10:11], v[220:221], v[36:37], v[10:11] op_sel_hi:[0,1,1]
	v_pk_fma_f32 v[12:13], v[220:221], v[52:53], v[12:13] op_sel_hi:[0,1,1]
	v_pk_fma_f32 v[14:15], v[220:221], v[68:69], v[14:15] op_sel_hi:[0,1,1]
	v_fmac_f32_e32 v16, v220, v86
	s_waitcnt vmcnt(12)
	v_pk_fma_f32 v[8:9], v[222:223], v[28:29], v[8:9] op_sel_hi:[0,1,1]
	v_pk_fma_f32 v[10:11], v[222:223], v[46:47], v[10:11] op_sel_hi:[0,1,1]
	v_pk_fma_f32 v[12:13], v[222:223], v[62:63], v[12:13] op_sel_hi:[0,1,1]
	v_pk_fma_f32 v[14:15], v[222:223], v[78:79], v[14:15] op_sel_hi:[0,1,1]
	v_fmac_f32_e32 v16, v222, v87
	s_waitcnt vmcnt(11)
	v_pk_fma_f32 v[8:9], v[224:225], v[70:71], v[8:9] op_sel_hi:[0,1,1]
	v_pk_fma_f32 v[10:11], v[224:225], v[24:25], v[10:11] op_sel_hi:[0,1,1]
	v_pk_fma_f32 v[12:13], v[224:225], v[42:43], v[12:13] op_sel_hi:[0,1,1]
	v_pk_fma_f32 v[14:15], v[224:225], v[58:59], v[14:15] op_sel_hi:[0,1,1]
	s_waitcnt lgkmcnt(0)
	v_fmac_f32_e32 v16, v224, v88
	s_waitcnt vmcnt(10)
	v_pk_fma_f32 v[8:9], v[226:227], v[30:31], v[8:9] op_sel_hi:[0,1,1]
	v_pk_fma_f32 v[10:11], v[226:227], v[48:49], v[10:11] op_sel_hi:[0,1,1]
	v_pk_fma_f32 v[12:13], v[226:227], v[64:65], v[12:13] op_sel_hi:[0,1,1]
	v_pk_fma_f32 v[14:15], v[226:227], v[80:81], v[14:15] op_sel_hi:[0,1,1]
	v_fmac_f32_e32 v16, v226, v89
	s_waitcnt vmcnt(9)
	v_pk_fma_f32 v[8:9], v[228:229], v[22:23], v[8:9] op_sel_hi:[0,1,1]
	v_pk_fma_f32 v[10:11], v[228:229], v[40:41], v[10:11] op_sel_hi:[0,1,1]
	v_pk_fma_f32 v[12:13], v[228:229], v[56:57], v[12:13] op_sel_hi:[0,1,1]
	v_pk_fma_f32 v[14:15], v[228:229], v[72:73], v[14:15] op_sel_hi:[0,1,1]
	v_fmac_f32_e32 v16, v228, v90
	s_waitcnt vmcnt(8)
; #define GAS __attribute__((address_space(1)))
; template <class T> __device__ __forceinline__ T* wsp(const Frame& F, size_t off) { return (T*)(F.ws + off); }
; #define NTLD(P) (NT_STREAMS ? __builtin_nontemporal_load(P) : *(P))
; __device__ __forceinline__ void p0_prologue(Frame& F) {
;     ...
; #pragma unroll 8
;             for (int kk = 0; kk < 128; ++kk) { const int k = F.wave * 128 + kk; const float w = NTLD((const GAS float*)(W + (size_t)k * 6144));
; #pragma unroll
;                 for (int r = 0; r < 9; ++r) a[r] += sc[r * 1024 + k] * w; }
; #pragma unroll
;             for (int r = 0; r < 9; ++r) part[(F.wave * 9 + r) * 64 + F.lane] = a[r];
;             __syncthreads();
;             for (int i = F.tid; i < 576; i += 512) { const int r = i >> 6, l = i & 63; float s = 0.f;
; #pragma unroll
;                 for (int w = 0; w < 8; ++w) s += part[(w * 9 + r) * 64 + l];
;                 const int cc = (item % 96) * 64 + l;
;                 wsp<float>(F, WS_MOD)[(size_t)(layer * 9 + r) * 6144 + cc] = s + inp(F, I_ADAB)[layer * 6144 + cc]; }
	v_pk_fma_f32 v[8:9], v[230:231], v[32:33], v[8:9] op_sel_hi:[0,1,1]
	v_pk_fma_f32 v[10:11], v[230:231], v[50:51], v[10:11] op_sel_hi:[0,1,1]
	v_pk_fma_f32 v[12:13], v[230:231], v[66:67], v[12:13] op_sel_hi:[0,1,1]
	v_pk_fma_f32 v[14:15], v[230:231], v[82:83], v[14:15] op_sel_hi:[0,1,1]
	v_fmac_f32_e32 v16, v230, v91
	v_mov_b32_e32 v17, s11
	ds_read_b128 v[18:21], v17
	ds_read_b128 v[22:25], v17 offset:16
	ds_read_b128 v[26:29], v17 offset:4096
	ds_read_b128 v[30:33], v17 offset:4112
	ds_read_b128 v[36:39], v17 offset:8192
	ds_read_b128 v[40:43], v17 offset:8208
	ds_read_b128 v[44:47], v17 offset:12288
	ds_read_b128 v[48:51], v17 offset:12304
	ds_read_b128 v[52:55], v17 offset:16384
	ds_read_b128 v[56:59], v17 offset:16400
	ds_read_b128 v[60:63], v17 offset:20480
	ds_read_b128 v[64:67], v17 offset:20496
	ds_read_b128 v[68:71], v17 offset:24576
	ds_read_b128 v[72:75], v17 offset:24592
	ds_read_b128 v[76:79], v17 offset:28672
	ds_read_b128 v[80:83], v17 offset:28688
	s_add_i32 s11, s11, 32
	ds_read_b128 v[84:87], v17 offset:32768
	ds_read_b128 v[88:91], v17 offset:32784
	s_waitcnt lgkmcnt(0)
	v_mov_b32_e32 v92, v18
	v_mov_b32_e32 v93, v26
	v_mov_b32_e32 v26, v19
	v_mov_b32_e32 v18, v20
	v_mov_b32_e32 v19, v28
	v_mov_b32_e32 v28, v21
	s_waitcnt lgkmcnt(13)
	v_mov_b32_e32 v20, v36
	s_waitcnt lgkmcnt(11)
	v_mov_b32_e32 v21, v44
	v_mov_b32_e32 v44, v37
	v_mov_b32_e32 v36, v38
	v_mov_b32_e32 v37, v46
	v_mov_b32_e32 v46, v39
	s_waitcnt lgkmcnt(9)
	v_mov_b32_e32 v38, v52
	s_waitcnt lgkmcnt(7)
	v_mov_b32_e32 v39, v60
	v_mov_b32_e32 v60, v53
	v_mov_b32_e32 v52, v54
	v_mov_b32_e32 v53, v62
	v_mov_b32_e32 v62, v55
	s_waitcnt lgkmcnt(5)
	v_mov_b32_e32 v54, v68
	s_waitcnt lgkmcnt(3)
	v_mov_b32_e32 v55, v76
	v_mov_b32_e32 v76, v69
	v_mov_b32_e32 v68, v70
	v_mov_b32_e32 v69, v78
	v_mov_b32_e32 v78, v71
	v_mov_b32_e32 v70, v22
	v_mov_b32_e32 v71, v30
	v_mov_b32_e32 v30, v23
	v_mov_b32_e32 v22, v24
	v_mov_b32_e32 v23, v32
	v_mov_b32_e32 v32, v25
	v_mov_b32_e32 v24, v40
	v_mov_b32_e32 v25, v48
	v_mov_b32_e32 v48, v41
	v_mov_b32_e32 v40, v42
	v_mov_b32_e32 v41, v50
	v_mov_b32_e32 v50, v43
	v_mov_b32_e32 v42, v56
	v_mov_b32_e32 v43, v64
	v_mov_b32_e32 v64, v57
	v_mov_b32_e32 v56, v58
	v_mov_b32_e32 v57, v66
	v_mov_b32_e32 v66, v59
	v_mov_b32_e32 v58, v72
	s_waitcnt lgkmcnt(2)
	v_mov_b32_e32 v59, v80
	v_mov_b32_e32 v80, v73
	v_mov_b32_e32 v72, v74
	v_mov_b32_e32 v73, v82
	v_mov_b32_e32 v82, v75
	s_waitcnt vmcnt(7)
	v_pk_fma_f32 v[8:9], v[232:233], v[92:93], v[8:9] op_sel_hi:[0,1,1]
	v_pk_fma_f32 v[10:11], v[232:233], v[20:21], v[10:11] op_sel_hi:[0,1,1]
	v_pk_fma_f32 v[12:13], v[232:233], v[38:39], v[12:13] op_sel_hi:[0,1,1]
	v_pk_fma_f32 v[14:15], v[232:233], v[54:55], v[14:15] op_sel_hi:[0,1,1]
	s_waitcnt lgkmcnt(1)
	v_fmac_f32_e32 v16, v232, v84
	s_waitcnt vmcnt(6)
	v_pk_fma_f32 v[8:9], v[234:235], v[26:27], v[8:9] op_sel_hi:[0,1,1]
	v_pk_fma_f32 v[10:11], v[234:235], v[44:45], v[10:11] op_sel_hi:[0,1,1]
	v_pk_fma_f32 v[12:13], v[234:235], v[60:61], v[12:13] op_sel_hi:[0,1,1]
	v_pk_fma_f32 v[14:15], v[234:235], v[76:77], v[14:15] op_sel_hi:[0,1,1]
	v_fmac_f32_e32 v16, v234, v85
	s_waitcnt vmcnt(5)
	v_pk_fma_f32 v[8:9], v[236:237], v[18:19], v[8:9] op_sel_hi:[0,1,1]
	v_pk_fma_f32 v[10:11], v[236:237], v[36:37], v[10:11] op_sel_hi:[0,1,1]
	v_pk_fma_f32 v[12:13], v[236:237], v[52:53], v[12:13] op_sel_hi:[0,1,1]
	v_pk_fma_f32 v[14:15], v[236:237], v[68:69], v[14:15] op_sel_hi:[0,1,1]
	v_fmac_f32_e32 v16, v236, v86
	s_waitcnt vmcnt(4)
	v_pk_fma_f32 v[8:9], v[238:239], v[28:29], v[8:9] op_sel_hi:[0,1,1]
	v_pk_fma_f32 v[10:11], v[238:239], v[46:47], v[10:11] op_sel_hi:[0,1,1]
	v_pk_fma_f32 v[12:13], v[238:239], v[62:63], v[12:13] op_sel_hi:[0,1,1]
	v_pk_fma_f32 v[14:15], v[238:239], v[78:79], v[14:15] op_sel_hi:[0,1,1]
	v_fmac_f32_e32 v16, v238, v87
	s_waitcnt vmcnt(3)
	v_pk_fma_f32 v[8:9], v[240:241], v[70:71], v[8:9] op_sel_hi:[0,1,1]
	v_pk_fma_f32 v[10:11], v[240:241], v[24:25], v[10:11] op_sel_hi:[0,1,1]
	v_pk_fma_f32 v[12:13], v[240:241], v[42:43], v[12:13] op_sel_hi:[0,1,1]
	v_pk_fma_f32 v[14:15], v[240:241], v[58:59], v[14:15] op_sel_hi:[0,1,1]
	s_waitcnt lgkmcnt(0)
	v_fmac_f32_e32 v16, v240, v88
	s_waitcnt vmcnt(2)
	v_pk_fma_f32 v[8:9], v[242:243], v[30:31], v[8:9] op_sel_hi:[0,1,1]
	v_pk_fma_f32 v[10:11], v[242:243], v[48:49], v[10:11] op_sel_hi:[0,1,1]
	v_pk_fma_f32 v[12:13], v[242:243], v[64:65], v[12:13] op_sel_hi:[0,1,1]
	v_pk_fma_f32 v[14:15], v[242:243], v[80:81], v[14:15] op_sel_hi:[0,1,1]
	v_fmac_f32_e32 v16, v242, v89
	s_waitcnt vmcnt(1)
	v_pk_fma_f32 v[8:9], v[244:245], v[22:23], v[8:9] op_sel_hi:[0,1,1]
	v_pk_fma_f32 v[10:11], v[244:245], v[40:41], v[10:11] op_sel_hi:[0,1,1]
	v_pk_fma_f32 v[12:13], v[244:245], v[56:57], v[12:13] op_sel_hi:[0,1,1]
	v_pk_fma_f32 v[14:15], v[244:245], v[72:73], v[14:15] op_sel_hi:[0,1,1]
	v_fmac_f32_e32 v16, v244, v90
	s_waitcnt vmcnt(0)
	v_pk_fma_f32 v[8:9], v[246:247], v[32:33], v[8:9] op_sel_hi:[0,1,1]
	v_pk_fma_f32 v[10:11], v[246:247], v[50:51], v[10:11] op_sel_hi:[0,1,1]
	v_pk_fma_f32 v[12:13], v[246:247], v[66:67], v[12:13] op_sel_hi:[0,1,1]
	v_pk_fma_f32 v[14:15], v[246:247], v[82:83], v[14:15] op_sel_hi:[0,1,1]
	v_fmac_f32_e32 v16, v246, v91
	v_add_u32_e32 v4, s12, v1
	ds_write2st64_b32 v4, v8, v9 offset0:160 offset1:161
	ds_write2st64_b32 v4, v10, v11 offset0:162 offset1:163
	ds_write2st64_b32 v4, v12, v13 offset0:164 offset1:165
	ds_write2st64_b32 v4, v14, v15 offset0:166 offset1:167
	ds_write_b32 v4, v16 offset:43008
	s_waitcnt lgkmcnt(0)
	s_barrier
	s_and_saveexec_b64 s[4:5], vcc
	s_cbranch_execz .LBB0_39
	v_mov_b32_e32 v4, s44
	ds_read_b64 v[4:5], v4
	s_mul_i32 s0, s10, 0x1800
	v_add_u32_e32 v8, s0, v2
	s_mul_i32 s45, s10, 9
	v_ashrrev_i32_e32 v9, 31, v8
	v_lshl_add_u64 v[2:3], v[2:3], 2, s[2:3]
	s_mov_b64 s[10:11], 0
	v_mov_b32_e32 v10, v6
